# P9/P19 down-GEMM epilogue: 8 gate loads hoisted to the top (1 wait instead of 8 load+vmcnt0 round trips), drop header vmcnt(0) drain and s_nop pads
# speedup vs baseline: 1.0057x; 1.0057x over previous
; #define PG8_STAGE(bufoff, gbase, voff) do { _Pragma("unroll") for (int _i = 0; _i < 2; ++_i) \
;         __builtin_amdgcn_global_load_lds((const unsigned*)((const char*)(gbase) + (voff)[_i]), (PG8_LAS unsigned*)(lds + (bufoff) + ldsw + _i * 8192), 16, 0, 0); } while (0)
; #define PG8_STAGE_A(bufoff, gbase, h, nx) do { if constexpr (Sched::GATHER) { const unsigned vv_[2] = {(nx) ? vAn[h][0] : vA[h][0], (nx) ? vAn[h][1] : vA[h][1]}; PG8_STAGE(bufoff, gbase, vv_); } \
;         else { PG8_STAGE(bufoff, (gbase) + (h) * hstep, voffA); } } while (0)
; #define PG8_LDA(dst, b, h) do { _Pragma("unroll") for (int m = 0; m < 4; ++m) _Pragma("unroll") for (int k = 0; k < 2; ++k) dst[m][k] = *(const PG8_LAS bf16x8*)(lds + PG8_SA(b, h) + aoff + m * 2048 + k * 1024); } while (0)
; #define PG8_WAIT_V(n) asm volatile("s_waitcnt vmcnt(" #n ")" ::: "memory")
; #define PG8_WAIT_L(n) asm volatile("s_waitcnt lgkmcnt(" #n ")" ::: "memory")
;     ...
;         const bool has_next = S.next(ui + 1, nxt);
;         const char* nA = Sched::GATHER ? cA : (has_next ? (const char*)g.A + (size_t)nxt.pm * tstep : cA);
;         if constexpr (Sched::GATHER) { if (has_next) { PG8_AOFF(vAn, ui + 1); } else { _Pragma("unroll") for (int h_ = 0; h_ < 2; ++h_) _Pragma("unroll") for (int i_ = 0; i_ < 2; ++i_) vAn[h_][i_] = vA[h_][i_]; } } const char* nB = has_next ? (const char*)g.Bt + (size_t)nxt.pb * tstep : cB;
; #pragma nounroll
;         for (int t = 0; t < nt; t += 2) {
;             const bool last = (t == nt - 2);
;             const char* a1 = cA + (size_t)(t + 1) * kstep;
;             const char* a2 = last ? nA : cA + (size_t)(t + 2) * kstep; const char* b2 = last ? nB : cB + (size_t)(t + 2) * kstep;
;             const char* a3 = a2 + kstep; const char* b3 = b2 + kstep;
;             if (last && has_next) S.a_ready(nxt);
;             if constexpr (SP2) {
;             PG8_LDB(B0, 0, 0); PG8_LDB(B1, 0, 1); PG8_SCHED; PG8_LDA(At, 0, 0); PG8_STAGE_A(PG8_SA(1, 1), a1, 1, false);
;             PG8_WAIT_V(8); PG8_WAIT_L(0); PG8_BAR; PG8_MMA(0, 0, At, B0); PG8_MMA(0, 1, At, B1); PG8_BAR; PG8_SCHED;
;             PG8_LDA(At, 0, 1); PG8_STAGE(PG8_SB(0, 0), b2, voffB); PG8_STAGE(PG8_SB(0, 1), b2 + hstepB, voffB); PG8_STAGE_A(PG8_SA(0, 0), a2, 0, last);
;             PG8_WAIT_V(8); PG8_WAIT_L(0); PG8_BAR; PG8_MMA(1, 0, At, B0); PG8_MMA(1, 1, At, B1); PG8_BAR; PG8_SCHED;
.LBB0_894:
	s_ashr_i32 s13, s12, 31
	s_lshl_b64 s[16:17], s[12:13], 19
	v_readlane_b32 s18, v255, 9
	v_readlane_b32 s19, v255, 10
	s_add_u32 s16, s18, s16
	s_addc_u32 s17, s19, s17
	s_and_b64 s[18:19], s[2:3], exec
	s_cselect_b32 s13, s17, s23
	s_cselect_b32 s21, s16, s22
	s_ashr_i32 s15, s14, 31
	s_lshl_b64 s[18:19], s[14:15], 19
	v_readlane_b32 s26, v254, 63
	v_readlane_b32 s27, v255, 0
	s_add_u32 s18, s26, s18
	s_addc_u32 s19, s27, s19
	s_and_b64 s[26:27], s[2:3], exec
	s_cselect_b32 s15, s19, s25
	s_cselect_b32 s44, s18, s24
	s_add_u32 s22, s22, 0x40080
	s_addc_u32 s23, s23, 0
	s_add_u32 s45, s24, 0x100
	s_addc_u32 s46, s25, 0
	s_mov_b32 s47, -2
	ds_read_b128 v[26:29], v188
	ds_read_b128 v[30:33], v188 offset:1024
	ds_read_b128 v[18:21], v188 offset:2048
	ds_read_b128 v[22:25], v188 offset:3072
	ds_read_b128 v[10:13], v189
	ds_read_b128 v[14:17], v189 offset:1024
	ds_read_b128 v[2:5], v189 offset:2048
	ds_read_b128 v[6:9], v189 offset:3072
	s_add_u32 s24, s22, 0xfffc0080
	s_addc_u32 s25, s23, -1
	s_cmp_eq_u32 s47, 12
	s_cselect_b32 s27, s13, s25
	s_cselect_b32 s26, s21, s24
	s_cselect_b32 s25, s15, s46
	s_cselect_b32 s24, s44, s45
	v_lshl_add_u64 v[218:219], s[22:23], 0, v[170:171]
	s_add_i32 m0, s29, 0xc000
	ds_read_b128 v[178:181], v190
	ds_read_b128 v[182:185], v190 offset:1024
	ds_read_b128 v[194:197], v190 offset:2048
	ds_read_b128 v[198:201], v190 offset:3072
	ds_read_b128 v[202:205], v190 offset:4096
	ds_read_b128 v[206:209], v190 offset:5120
	ds_read_b128 v[210:213], v190 offset:6144
	ds_read_b128 v[214:217], v190 offset:7168
	global_load_lds_dwordx4 v[218:219], off
	v_lshl_add_u64 v[218:219], s[22:23], 0, v[172:173]
	s_add_i32 m0, s29, 0xe000
	s_nop 0
	global_load_lds_dwordx4 v[218:219], off
	s_waitcnt vmcnt(8)
	s_waitcnt lgkmcnt(0)
	s_barrier
	s_setprio 1
	s_nop 3
	s_waitcnt lgkmcnt(0)
	v_mfma_scale_f32_16x16x128_f8f6f4 v[158:161], v[26:33], v[178:185], 0, v191, v192 op_sel_hi:[0,0,0]
	v_mfma_scale_f32_16x16x128_f8f6f4 v[154:157], v[18:25], v[178:185], 0, v191, v192 op_sel_hi:[0,0,0]
	v_mfma_scale_f32_16x16x128_f8f6f4 v[142:145], v[26:33], v[194:201], 0, v191, v192 op_sel_hi:[0,0,0]
	v_mfma_scale_f32_16x16x128_f8f6f4 v[138:141], v[18:25], v[194:201], 0, v191, v192 op_sel_hi:[0,0,0]
	v_mfma_scale_f32_16x16x128_f8f6f4 v[126:129], v[26:33], v[202:209], 0, v191, v192 op_sel_hi:[0,0,0]
	v_mfma_scale_f32_16x16x128_f8f6f4 v[122:125], v[18:25], v[202:209], 0, v191, v192 op_sel_hi:[0,0,0]
	v_mfma_scale_f32_16x16x128_f8f6f4 v[110:113], v[26:33], v[210:217], 0, v191, v192 op_sel_hi:[0,0,0]
	v_mfma_scale_f32_16x16x128_f8f6f4 v[106:109], v[18:25], v[210:217], 0, v191, v192 op_sel_hi:[0,0,0]
	s_setprio 0
	s_setprio 1
	s_nop 3
	v_mfma_scale_f32_16x16x128_f8f6f4 v[150:153], v[10:17], v[178:185], 0, v191, v192 op_sel_hi:[0,0,0]
	v_mfma_scale_f32_16x16x128_f8f6f4 v[146:149], v[2:9], v[178:185], 0, v191, v192 op_sel_hi:[0,0,0]
	v_mfma_scale_f32_16x16x128_f8f6f4 v[134:137], v[10:17], v[194:201], 0, v191, v192 op_sel_hi:[0,0,0]
	v_mfma_scale_f32_16x16x128_f8f6f4 v[130:133], v[2:9], v[194:201], 0, v191, v192 op_sel_hi:[0,0,0]
	v_mfma_scale_f32_16x16x128_f8f6f4 v[118:121], v[10:17], v[202:209], 0, v191, v192 op_sel_hi:[0,0,0]
	v_mfma_scale_f32_16x16x128_f8f6f4 v[114:117], v[2:9], v[202:209], 0, v191, v192 op_sel_hi:[0,0,0]
	v_mfma_scale_f32_16x16x128_f8f6f4 v[102:105], v[10:17], v[210:217], 0, v191, v192 op_sel_hi:[0,0,0]
	v_mfma_scale_f32_16x16x128_f8f6f4 v[98:101], v[2:9], v[210:217], 0, v191, v192 op_sel_hi:[0,0,0]
	s_setprio 0
	s_barrier
	s_add_i32 s48, s40, s28
	v_lshl_add_u64 v[178:179], s[24:25], 0, v[166:167]
	s_mov_b32 m0, s48
	ds_read_b128 v[194:197], v190 offset:16384
	ds_read_b128 v[198:201], v190 offset:17408
	ds_read_b128 v[202:205], v190 offset:18432
	ds_read_b128 v[206:209], v190 offset:19456
	ds_read_b128 v[210:213], v190 offset:20480
	ds_read_b128 v[214:217], v190 offset:21504
	ds_read_b128 v[218:221], v190 offset:22528
	ds_read_b128 v[222:225], v190 offset:23552
	global_load_lds_dwordx4 v[178:179], off
	s_add_i32 m0, s48, 0x2000
	s_add_u32 s48, s24, 0x4000
	v_lshl_add_u64 v[180:181], s[24:25], 0, v[162:163]
	s_addc_u32 s49, s25, 0
	s_add_i32 s50, s41, s28
	global_load_lds_dwordx4 v[180:181], off
	v_lshl_add_u64 v[182:183], s[48:49], 0, v[166:167]
	s_mov_b32 m0, s50
	v_lshl_add_u64 v[184:185], s[26:27], 0, v[164:165]
	global_load_lds_dwordx4 v[182:183], off
	v_lshl_add_u64 v[182:183], s[48:49], 0, v[162:163]
	s_add_i32 m0, s50, 0x2000
	s_nop 0
	global_load_lds_dwordx4 v[182:183], off
	v_lshl_add_u64 v[182:183], s[26:27], 0, v[168:169]
	s_mov_b32 m0, s29
	s_nop 0
	global_load_lds_dwordx4 v[182:183], off
	s_mov_b32 m0, s30
	s_nop 0
	global_load_lds_dwordx4 v[184:185], off
	s_waitcnt vmcnt(8)
	s_waitcnt lgkmcnt(0)
	s_barrier
	s_setprio 1
	s_nop 3
	s_waitcnt lgkmcnt(0)
	v_mfma_scale_f32_16x16x128_f8f6f4 v[94:97], v[26:33], v[194:201], 0, v191, v192 op_sel_hi:[0,0,0]
	v_mfma_scale_f32_16x16x128_f8f6f4 v[90:93], v[18:25], v[194:201], 0, v191, v192 op_sel_hi:[0,0,0]
	v_mfma_scale_f32_16x16x128_f8f6f4 v[78:81], v[26:33], v[202:209], 0, v191, v192 op_sel_hi:[0,0,0]
	v_mfma_scale_f32_16x16x128_f8f6f4 v[74:77], v[18:25], v[202:209], 0, v191, v192 op_sel_hi:[0,0,0]
	v_mfma_scale_f32_16x16x128_f8f6f4 v[62:65], v[26:33], v[210:217], 0, v191, v192 op_sel_hi:[0,0,0]
	v_mfma_scale_f32_16x16x128_f8f6f4 v[58:61], v[18:25], v[210:217], 0, v191, v192 op_sel_hi:[0,0,0]
	v_mfma_scale_f32_16x16x128_f8f6f4 v[46:49], v[26:33], v[218:225], 0, v191, v192 op_sel_hi:[0,0,0]
	v_mfma_scale_f32_16x16x128_f8f6f4 v[42:45], v[18:25], v[218:225], 0, v191, v192 op_sel_hi:[0,0,0]
	s_setprio 0
	s_setprio 1
	s_nop 3
	v_mfma_scale_f32_16x16x128_f8f6f4 v[86:89], v[10:17], v[194:201], 0, v191, v192 op_sel_hi:[0,0,0]
	v_mfma_scale_f32_16x16x128_f8f6f4 v[82:85], v[2:9], v[194:201], 0, v191, v192 op_sel_hi:[0,0,0]
	v_mfma_scale_f32_16x16x128_f8f6f4 v[70:73], v[10:17], v[202:209], 0, v191, v192 op_sel_hi:[0,0,0]
	v_mfma_scale_f32_16x16x128_f8f6f4 v[66:69], v[2:9], v[202:209], 0, v191, v192 op_sel_hi:[0,0,0]
	v_mfma_scale_f32_16x16x128_f8f6f4 v[54:57], v[10:17], v[210:217], 0, v191, v192 op_sel_hi:[0,0,0]
	v_mfma_scale_f32_16x16x128_f8f6f4 v[50:53], v[2:9], v[210:217], 0, v191, v192 op_sel_hi:[0,0,0]
	v_mfma_scale_f32_16x16x128_f8f6f4 v[38:41], v[10:17], v[218:225], 0, v191, v192 op_sel_hi:[0,0,0]
	v_mfma_scale_f32_16x16x128_f8f6f4 v[34:37], v[2:9], v[218:225], 0, v191, v192 op_sel_hi:[0,0,0]
	s_setprio 0
	s_barrier
; #define PG8_STAGE(bufoff, gbase, voff) do { _Pragma("unroll") for (int _i = 0; _i < 2; ++_i) \
;         __builtin_amdgcn_global_load_lds((const unsigned*)((const char*)(gbase) + (voff)[_i]), (PG8_LAS unsigned*)(lds + (bufoff) + ldsw + _i * 8192), 16, 0, 0); } while (0)
; #define PG8_STAGE_A(bufoff, gbase, h, nx) do { if constexpr (Sched::GATHER) { const unsigned vv_[2] = {(nx) ? vAn[h][0] : vA[h][0], (nx) ? vAn[h][1] : vA[h][1]}; PG8_STAGE(bufoff, gbase, vv_); } \
;         else { PG8_STAGE(bufoff, (gbase) + (h) * hstep, voffA); } } while (0)
; #define PG8_LDA(dst, b, h) do { _Pragma("unroll") for (int m = 0; m < 4; ++m) _Pragma("unroll") for (int k = 0; k < 2; ++k) dst[m][k] = *(const PG8_LAS bf16x8*)(lds + PG8_SA(b, h) + aoff + m * 2048 + k * 1024); } while (0)
; #define PG8_LDB(dst, b, h) do { _Pragma("unroll") for (int n = 0; n < 2; ++n) _Pragma("unroll") for (int k = 0; k < 2; ++k) dst[n][k] = *(const PG8_LAS bf16x8*)(lds + PG8_SB(b, h) + boff + n * 2048 + k * 1024); } while (0)
; #define PG8_WAIT_V(n) asm volatile("s_waitcnt vmcnt(" #n ")" ::: "memory")
; #define PG8_WAIT_L(n) asm volatile("s_waitcnt lgkmcnt(" #n ")" ::: "memory")
; #define PG8_BAR __builtin_amdgcn_s_barrier()
; #define PG8_SCHED __builtin_amdgcn_sched_barrier(0)
;     ...
;             PG8_LDB(B0, 1, 0); PG8_LDB(B1, 1, 1); PG8_SCHED; PG8_LDA(At, 1, 0); PG8_STAGE_A(PG8_SA(0, 1), a2, 1, last);
;             PG8_WAIT_V(8); PG8_WAIT_L(0); PG8_BAR; PG8_MMA(0, 0, At, B0); PG8_MMA(0, 1, At, B1); PG8_BAR; PG8_SCHED;
;             PG8_LDA(At, 1, 1); PG8_STAGE(PG8_SB(1, 0), b3, voffB); PG8_STAGE(PG8_SB(1, 1), b3 + hstepB, voffB); PG8_STAGE_A(PG8_SA(1, 0), a3, 0, last);
;             PG8_WAIT_V(8); PG8_WAIT_L(0); PG8_BAR; PG8_MMA(1, 0, At, B0); PG8_MMA(1, 1, At, B1); PG8_BAR; PG8_SCHED;
	s_add_i32 s48, 0, 0x18000
	s_add_i32 s49, 0, 0x1c000
	v_add_u32_e32 v14, s48, v186
	v_add_u32_e32 v30, s49, v186
	ds_read_b128 v[2:5], v14
	ds_read_b128 v[6:9], v14 offset:1024
	ds_read_b128 v[10:13], v14 offset:2048
	ds_read_b128 v[14:17], v14 offset:3072
	ds_read_b128 v[18:21], v30
	ds_read_b128 v[22:25], v30 offset:1024
	ds_read_b128 v[26:29], v30 offset:2048
	ds_read_b128 v[30:33], v30 offset:3072
	s_add_u32 s26, s26, 0x40000
	s_addc_u32 s27, s27, 0
	s_mov_b32 m0, s31
	v_lshl_add_u64 v[226:227], s[26:27], 0, v[168:169]
	ds_read_b128 v[194:197], v190 offset:32768
	ds_read_b128 v[198:201], v190 offset:33792
	ds_read_b128 v[202:205], v190 offset:34816
	ds_read_b128 v[206:209], v190 offset:35840
	ds_read_b128 v[210:213], v190 offset:36864
	ds_read_b128 v[214:217], v190 offset:37888
	ds_read_b128 v[218:221], v190 offset:38912
	ds_read_b128 v[222:225], v190 offset:39936
	global_load_lds_dwordx4 v[226:227], off
	v_lshl_add_u64 v[226:227], s[26:27], 0, v[164:165]
	s_mov_b32 m0, s34
	s_nop 0
	global_load_lds_dwordx4 v[226:227], off
	s_waitcnt vmcnt(8)
	s_waitcnt lgkmcnt(0)
	s_barrier
	s_setprio 1
	s_nop 3
	s_waitcnt lgkmcnt(0)
	v_mfma_scale_f32_16x16x128_f8f6f4 v[158:161], v[2:9], v[194:201], v[158:161], v191, v192 op_sel_hi:[0,0,0]
	v_mfma_scale_f32_16x16x128_f8f6f4 v[154:157], v[10:17], v[194:201], v[154:157], v191, v192 op_sel_hi:[0,0,0]
	v_mfma_scale_f32_16x16x128_f8f6f4 v[142:145], v[2:9], v[202:209], v[142:145], v191, v192 op_sel_hi:[0,0,0]
	v_mfma_scale_f32_16x16x128_f8f6f4 v[138:141], v[10:17], v[202:209], v[138:141], v191, v192 op_sel_hi:[0,0,0]
	v_mfma_scale_f32_16x16x128_f8f6f4 v[126:129], v[2:9], v[210:217], v[126:129], v191, v192 op_sel_hi:[0,0,0]
	v_mfma_scale_f32_16x16x128_f8f6f4 v[122:125], v[10:17], v[210:217], v[122:125], v191, v192 op_sel_hi:[0,0,0]
	v_mfma_scale_f32_16x16x128_f8f6f4 v[110:113], v[2:9], v[218:225], v[110:113], v191, v192 op_sel_hi:[0,0,0]
	v_mfma_scale_f32_16x16x128_f8f6f4 v[106:109], v[10:17], v[218:225], v[106:109], v191, v192 op_sel_hi:[0,0,0]
	s_setprio 0
	s_setprio 1
	s_nop 3
	v_mfma_scale_f32_16x16x128_f8f6f4 v[150:153], v[18:25], v[194:201], v[150:153], v191, v192 op_sel_hi:[0,0,0]
	v_mfma_scale_f32_16x16x128_f8f6f4 v[146:149], v[26:33], v[194:201], v[146:149], v191, v192 op_sel_hi:[0,0,0]
	v_mfma_scale_f32_16x16x128_f8f6f4 v[134:137], v[18:25], v[202:209], v[134:137], v191, v192 op_sel_hi:[0,0,0]
	v_mfma_scale_f32_16x16x128_f8f6f4 v[130:133], v[26:33], v[202:209], v[130:133], v191, v192 op_sel_hi:[0,0,0]
	v_mfma_scale_f32_16x16x128_f8f6f4 v[118:121], v[18:25], v[210:217], v[118:121], v191, v192 op_sel_hi:[0,0,0]
	v_mfma_scale_f32_16x16x128_f8f6f4 v[114:117], v[26:33], v[210:217], v[114:117], v191, v192 op_sel_hi:[0,0,0]
	v_mfma_scale_f32_16x16x128_f8f6f4 v[102:105], v[18:25], v[218:225], v[102:105], v191, v192 op_sel_hi:[0,0,0]
	v_mfma_scale_f32_16x16x128_f8f6f4 v[98:101], v[26:33], v[218:225], v[98:101], v191, v192 op_sel_hi:[0,0,0]
	s_setprio 0
	s_barrier
	s_add_i32 s26, s48, s28
	v_lshl_add_u64 v[178:179], v[178:179], 0, s[8:9]
	s_mov_b32 m0, s26
	ds_read_b128 v[194:197], v190 offset:49152
	ds_read_b128 v[198:201], v190 offset:50176
	ds_read_b128 v[202:205], v190 offset:51200
	ds_read_b128 v[206:209], v190 offset:52224
	ds_read_b128 v[210:213], v190 offset:53248
	ds_read_b128 v[214:217], v190 offset:54272
	ds_read_b128 v[218:221], v190 offset:55296
	ds_read_b128 v[222:225], v190 offset:56320
	global_load_lds_dwordx4 v[178:179], off
	s_add_i32 m0, s26, 0x2000
	s_add_u32 s24, s24, 0x4080
	v_lshl_add_u64 v[178:179], v[180:181], 0, s[8:9]
	s_addc_u32 s25, s25, 0
	s_add_i32 s26, s49, s28
	global_load_lds_dwordx4 v[178:179], off
	v_lshl_add_u64 v[178:179], s[24:25], 0, v[166:167]
	s_mov_b32 m0, s26
	s_nop 0
	global_load_lds_dwordx4 v[178:179], off
	v_lshl_add_u64 v[178:179], s[24:25], 0, v[162:163]
	s_add_i32 m0, s26, 0x2000
	s_nop 0
	global_load_lds_dwordx4 v[178:179], off
	v_lshl_add_u64 v[178:179], v[182:183], 0, s[8:9]
	s_mov_b32 m0, s38
	s_nop 0
	global_load_lds_dwordx4 v[178:179], off
	v_lshl_add_u64 v[178:179], v[184:185], 0, s[8:9]
	s_mov_b32 m0, s39
	s_nop 0
	global_load_lds_dwordx4 v[178:179], off
	s_waitcnt vmcnt(8)
	s_waitcnt lgkmcnt(0)
	s_barrier
	s_setprio 1
	s_nop 3
	s_waitcnt lgkmcnt(0)
	v_mfma_scale_f32_16x16x128_f8f6f4 v[94:97], v[2:9], v[194:201], v[94:97], v191, v192 op_sel_hi:[0,0,0]
	v_mfma_scale_f32_16x16x128_f8f6f4 v[90:93], v[10:17], v[194:201], v[90:93], v191, v192 op_sel_hi:[0,0,0]
	v_mfma_scale_f32_16x16x128_f8f6f4 v[78:81], v[2:9], v[202:209], v[78:81], v191, v192 op_sel_hi:[0,0,0]
	v_mfma_scale_f32_16x16x128_f8f6f4 v[74:77], v[10:17], v[202:209], v[74:77], v191, v192 op_sel_hi:[0,0,0]
	v_mfma_scale_f32_16x16x128_f8f6f4 v[62:65], v[2:9], v[210:217], v[62:65], v191, v192 op_sel_hi:[0,0,0]
	v_mfma_scale_f32_16x16x128_f8f6f4 v[58:61], v[10:17], v[210:217], v[58:61], v191, v192 op_sel_hi:[0,0,0]
	v_mfma_scale_f32_16x16x128_f8f6f4 v[46:49], v[2:9], v[218:225], v[46:49], v191, v192 op_sel_hi:[0,0,0]
	v_mfma_scale_f32_16x16x128_f8f6f4 v[42:45], v[10:17], v[218:225], v[42:45], v191, v192 op_sel_hi:[0,0,0]
	s_setprio 0
	s_setprio 1
	s_nop 3
	v_mfma_scale_f32_16x16x128_f8f6f4 v[86:89], v[18:25], v[194:201], v[86:89], v191, v192 op_sel_hi:[0,0,0]
	v_mfma_scale_f32_16x16x128_f8f6f4 v[82:85], v[26:33], v[194:201], v[82:85], v191, v192 op_sel_hi:[0,0,0]
	v_mfma_scale_f32_16x16x128_f8f6f4 v[70:73], v[18:25], v[202:209], v[70:73], v191, v192 op_sel_hi:[0,0,0]
	v_mfma_scale_f32_16x16x128_f8f6f4 v[66:69], v[26:33], v[202:209], v[66:69], v191, v192 op_sel_hi:[0,0,0]
	v_mfma_scale_f32_16x16x128_f8f6f4 v[54:57], v[18:25], v[210:217], v[54:57], v191, v192 op_sel_hi:[0,0,0]
	v_mfma_scale_f32_16x16x128_f8f6f4 v[50:53], v[26:33], v[210:217], v[50:53], v191, v192 op_sel_hi:[0,0,0]
	v_mfma_scale_f32_16x16x128_f8f6f4 v[38:41], v[18:25], v[218:225], v[38:41], v191, v192 op_sel_hi:[0,0,0]
	v_mfma_scale_f32_16x16x128_f8f6f4 v[34:37], v[26:33], v[218:225], v[34:37], v191, v192 op_sel_hi:[0,0,0]
	s_setprio 0
	s_barrier
	s_add_i32 s47, s47, 2
	s_add_u32 s22, s22, 0x100
	s_addc_u32 s23, s23, 0
	s_add_u32 s45, s45, 0x100
	s_addc_u32 s46, s46, 0
; #define PG8_STAGE(bufoff, gbase, voff) do { _Pragma("unroll") for (int _i = 0; _i < 2; ++_i) \
;         __builtin_amdgcn_global_load_lds((const unsigned*)((const char*)(gbase) + (voff)[_i]), (PG8_LAS unsigned*)(lds + (bufoff) + ldsw + _i * 8192), 16, 0, 0); } while (0)
; #define PG8_STAGE_A(bufoff, gbase, h, nx) do { if constexpr (Sched::GATHER) { const unsigned vv_[2] = {(nx) ? vAn[h][0] : vA[h][0], (nx) ? vAn[h][1] : vA[h][1]}; PG8_STAGE(bufoff, gbase, vv_); } \
;         else { PG8_STAGE(bufoff, (gbase) + (h) * hstep, voffA); } } while (0)
; #define PG8_LDA(dst, b, h) do { _Pragma("unroll") for (int m = 0; m < 4; ++m) _Pragma("unroll") for (int k = 0; k < 2; ++k) dst[m][k] = *(const PG8_LAS bf16x8*)(lds + PG8_SA(b, h) + aoff + m * 2048 + k * 1024); } while (0)
; #define PG8_LDB(dst, b, h) do { _Pragma("unroll") for (int n = 0; n < 2; ++n) _Pragma("unroll") for (int k = 0; k < 2; ++k) dst[n][k] = *(const PG8_LAS bf16x8*)(lds + PG8_SB(b, h) + boff + n * 2048 + k * 1024); } while (0)
; #define PG8_WAIT_V(n) asm volatile("s_waitcnt vmcnt(" #n ")" ::: "memory")
; #define PG8_WAIT_L(n) asm volatile("s_waitcnt lgkmcnt(" #n ")" ::: "memory")
; #define PG8_BAR __builtin_amdgcn_s_barrier()
; #define PG8_SCHED __builtin_amdgcn_sched_barrier(0)
;     ...
;         for (int t = 0; t < nt; t += 2) {
;             const bool last = (t == nt - 2);
;             const char* a1 = cA + (size_t)(t + 1) * kstep;
;             const char* a2 = last ? nA : cA + (size_t)(t + 2) * kstep; const char* b2 = last ? nB : cB + (size_t)(t + 2) * kstep;
;             const char* a3 = a2 + kstep; const char* b3 = b2 + kstep;
;             if (last && has_next) S.a_ready(nxt);
;             if constexpr (SP2) {
;             PG8_LDB(B0, 0, 0); PG8_LDB(B1, 0, 1); PG8_SCHED; PG8_LDA(At, 0, 0); PG8_STAGE_A(PG8_SA(1, 1), a1, 1, false);
;             PG8_WAIT_V(8); PG8_WAIT_L(0); PG8_BAR; PG8_MMA(0, 0, At, B0); PG8_MMA(0, 1, At, B1); PG8_BAR; PG8_SCHED;
;             PG8_LDA(At, 0, 1); PG8_STAGE(PG8_SB(0, 0), b2, voffB); PG8_STAGE(PG8_SB(0, 1), b2 + hstepB, voffB); PG8_STAGE_A(PG8_SA(0, 0), a2, 0, last);
;             PG8_WAIT_V(8); PG8_WAIT_L(0); PG8_BAR; PG8_MMA(1, 0, At, B0); PG8_MMA(1, 1, At, B1); PG8_BAR; PG8_SCHED;
.LBB0_895:
	ds_read_b128 v[26:29], v188
	ds_read_b128 v[30:33], v188 offset:1024
	ds_read_b128 v[18:21], v188 offset:2048
	ds_read_b128 v[22:25], v188 offset:3072
	ds_read_b128 v[10:13], v189
	ds_read_b128 v[14:17], v189 offset:1024
	ds_read_b128 v[2:5], v189 offset:2048
	ds_read_b128 v[6:9], v189 offset:3072
	s_add_u32 s24, s22, 0xfffc0080
	s_addc_u32 s25, s23, -1
	s_cmp_eq_u32 s47, 12
	s_cselect_b32 s27, s13, s25
	s_cselect_b32 s26, s21, s24
	s_cselect_b32 s25, s15, s46
	s_cselect_b32 s24, s44, s45
	v_lshl_add_u64 v[218:219], s[22:23], 0, v[170:171]
	s_add_i32 m0, s29, 0xc000
	ds_read_b128 v[178:181], v190
	ds_read_b128 v[182:185], v190 offset:1024
	ds_read_b128 v[194:197], v190 offset:2048
	ds_read_b128 v[198:201], v190 offset:3072
	ds_read_b128 v[202:205], v190 offset:4096
	ds_read_b128 v[206:209], v190 offset:5120
	ds_read_b128 v[210:213], v190 offset:6144
	ds_read_b128 v[214:217], v190 offset:7168
	global_load_lds_dwordx4 v[218:219], off
	v_lshl_add_u64 v[218:219], s[22:23], 0, v[172:173]
	s_add_i32 m0, s29, 0xe000
	s_nop 0
	global_load_lds_dwordx4 v[218:219], off
	s_waitcnt vmcnt(8)
	s_waitcnt lgkmcnt(0)
	s_barrier
	s_setprio 1
	s_nop 3
	s_waitcnt lgkmcnt(0)
	v_mfma_scale_f32_16x16x128_f8f6f4 v[158:161], v[26:33], v[178:185], v[158:161], v191, v192 op_sel_hi:[0,0,0]
	v_mfma_scale_f32_16x16x128_f8f6f4 v[154:157], v[18:25], v[178:185], v[154:157], v191, v192 op_sel_hi:[0,0,0]
	v_mfma_scale_f32_16x16x128_f8f6f4 v[142:145], v[26:33], v[194:201], v[142:145], v191, v192 op_sel_hi:[0,0,0]
	v_mfma_scale_f32_16x16x128_f8f6f4 v[138:141], v[18:25], v[194:201], v[138:141], v191, v192 op_sel_hi:[0,0,0]
	v_mfma_scale_f32_16x16x128_f8f6f4 v[126:129], v[26:33], v[202:209], v[126:129], v191, v192 op_sel_hi:[0,0,0]
	v_mfma_scale_f32_16x16x128_f8f6f4 v[122:125], v[18:25], v[202:209], v[122:125], v191, v192 op_sel_hi:[0,0,0]
	v_mfma_scale_f32_16x16x128_f8f6f4 v[110:113], v[26:33], v[210:217], v[110:113], v191, v192 op_sel_hi:[0,0,0]
	v_mfma_scale_f32_16x16x128_f8f6f4 v[106:109], v[18:25], v[210:217], v[106:109], v191, v192 op_sel_hi:[0,0,0]
	s_setprio 0
	s_setprio 1
	s_nop 3
	v_mfma_scale_f32_16x16x128_f8f6f4 v[150:153], v[10:17], v[178:185], v[150:153], v191, v192 op_sel_hi:[0,0,0]
	v_mfma_scale_f32_16x16x128_f8f6f4 v[146:149], v[2:9], v[178:185], v[146:149], v191, v192 op_sel_hi:[0,0,0]
	v_mfma_scale_f32_16x16x128_f8f6f4 v[134:137], v[10:17], v[194:201], v[134:137], v191, v192 op_sel_hi:[0,0,0]
	v_mfma_scale_f32_16x16x128_f8f6f4 v[130:133], v[2:9], v[194:201], v[130:133], v191, v192 op_sel_hi:[0,0,0]
	v_mfma_scale_f32_16x16x128_f8f6f4 v[118:121], v[10:17], v[202:209], v[118:121], v191, v192 op_sel_hi:[0,0,0]
	v_mfma_scale_f32_16x16x128_f8f6f4 v[114:117], v[2:9], v[202:209], v[114:117], v191, v192 op_sel_hi:[0,0,0]
	v_mfma_scale_f32_16x16x128_f8f6f4 v[102:105], v[10:17], v[210:217], v[102:105], v191, v192 op_sel_hi:[0,0,0]
	v_mfma_scale_f32_16x16x128_f8f6f4 v[98:101], v[2:9], v[210:217], v[98:101], v191, v192 op_sel_hi:[0,0,0]
	s_setprio 0
	s_barrier
	s_add_i32 s48, s40, s28
	v_lshl_add_u64 v[178:179], s[24:25], 0, v[166:167]
	s_mov_b32 m0, s48
	ds_read_b128 v[194:197], v190 offset:16384
	ds_read_b128 v[198:201], v190 offset:17408
	ds_read_b128 v[202:205], v190 offset:18432
	ds_read_b128 v[206:209], v190 offset:19456
	ds_read_b128 v[210:213], v190 offset:20480
	ds_read_b128 v[214:217], v190 offset:21504
	ds_read_b128 v[218:221], v190 offset:22528
	ds_read_b128 v[222:225], v190 offset:23552
	global_load_lds_dwordx4 v[178:179], off
	s_add_i32 m0, s48, 0x2000
	s_add_u32 s48, s24, 0x4000
	v_lshl_add_u64 v[180:181], s[24:25], 0, v[162:163]
	s_addc_u32 s49, s25, 0
	s_add_i32 s50, s41, s28
	global_load_lds_dwordx4 v[180:181], off
	v_lshl_add_u64 v[182:183], s[48:49], 0, v[166:167]
	s_mov_b32 m0, s50
	v_lshl_add_u64 v[184:185], s[26:27], 0, v[164:165]
	global_load_lds_dwordx4 v[182:183], off
	v_lshl_add_u64 v[182:183], s[48:49], 0, v[162:163]
	s_add_i32 m0, s50, 0x2000
	s_nop 0
	global_load_lds_dwordx4 v[182:183], off
	v_lshl_add_u64 v[182:183], s[26:27], 0, v[168:169]
	s_mov_b32 m0, s29
	s_nop 0
	global_load_lds_dwordx4 v[182:183], off
	s_mov_b32 m0, s30
	s_nop 0
	global_load_lds_dwordx4 v[184:185], off
	s_waitcnt vmcnt(8)
	s_waitcnt lgkmcnt(0)
	s_barrier
	s_setprio 1
	s_nop 3
	s_waitcnt lgkmcnt(0)
	v_mfma_scale_f32_16x16x128_f8f6f4 v[94:97], v[26:33], v[194:201], v[94:97], v191, v192 op_sel_hi:[0,0,0]
	v_mfma_scale_f32_16x16x128_f8f6f4 v[90:93], v[18:25], v[194:201], v[90:93], v191, v192 op_sel_hi:[0,0,0]
	v_mfma_scale_f32_16x16x128_f8f6f4 v[78:81], v[26:33], v[202:209], v[78:81], v191, v192 op_sel_hi:[0,0,0]
	v_mfma_scale_f32_16x16x128_f8f6f4 v[74:77], v[18:25], v[202:209], v[74:77], v191, v192 op_sel_hi:[0,0,0]
	v_mfma_scale_f32_16x16x128_f8f6f4 v[62:65], v[26:33], v[210:217], v[62:65], v191, v192 op_sel_hi:[0,0,0]
	v_mfma_scale_f32_16x16x128_f8f6f4 v[58:61], v[18:25], v[210:217], v[58:61], v191, v192 op_sel_hi:[0,0,0]
	v_mfma_scale_f32_16x16x128_f8f6f4 v[46:49], v[26:33], v[218:225], v[46:49], v191, v192 op_sel_hi:[0,0,0]
	v_mfma_scale_f32_16x16x128_f8f6f4 v[42:45], v[18:25], v[218:225], v[42:45], v191, v192 op_sel_hi:[0,0,0]
	s_setprio 0
	s_setprio 1
	s_nop 3
	v_mfma_scale_f32_16x16x128_f8f6f4 v[86:89], v[10:17], v[194:201], v[86:89], v191, v192 op_sel_hi:[0,0,0]
	v_mfma_scale_f32_16x16x128_f8f6f4 v[82:85], v[2:9], v[194:201], v[82:85], v191, v192 op_sel_hi:[0,0,0]
	v_mfma_scale_f32_16x16x128_f8f6f4 v[70:73], v[10:17], v[202:209], v[70:73], v191, v192 op_sel_hi:[0,0,0]
	v_mfma_scale_f32_16x16x128_f8f6f4 v[66:69], v[2:9], v[202:209], v[66:69], v191, v192 op_sel_hi:[0,0,0]
	v_mfma_scale_f32_16x16x128_f8f6f4 v[54:57], v[10:17], v[210:217], v[54:57], v191, v192 op_sel_hi:[0,0,0]
	v_mfma_scale_f32_16x16x128_f8f6f4 v[50:53], v[2:9], v[210:217], v[50:53], v191, v192 op_sel_hi:[0,0,0]
	v_mfma_scale_f32_16x16x128_f8f6f4 v[38:41], v[10:17], v[218:225], v[38:41], v191, v192 op_sel_hi:[0,0,0]
	v_mfma_scale_f32_16x16x128_f8f6f4 v[34:37], v[2:9], v[218:225], v[34:37], v191, v192 op_sel_hi:[0,0,0]
	s_setprio 0
	s_barrier
; #define PG8_STAGE(bufoff, gbase, voff) do { _Pragma("unroll") for (int _i = 0; _i < 2; ++_i) \
;         __builtin_amdgcn_global_load_lds((const unsigned*)((const char*)(gbase) + (voff)[_i]), (PG8_LAS unsigned*)(lds + (bufoff) + ldsw + _i * 8192), 16, 0, 0); } while (0)
; #define PG8_WAIT_V(n) asm volatile("s_waitcnt vmcnt(" #n ")" ::: "memory")
; #define PG8_WAIT_L(n) asm volatile("s_waitcnt lgkmcnt(" #n ")" ::: "memory")
;     ...
;             PG8_LDB(B0, 1, 0); PG8_LDB(B1, 1, 1); PG8_SCHED; PG8_LDA(At, 1, 0); PG8_STAGE_A(PG8_SA(0, 1), a2, 1, last);
;             PG8_WAIT_V(8); PG8_WAIT_L(0); PG8_BAR; PG8_MMA(0, 0, At, B0); PG8_MMA(0, 1, At, B1); PG8_BAR; PG8_SCHED;
;             PG8_LDA(At, 1, 1); PG8_STAGE(PG8_SB(1, 0), b3, voffB); PG8_STAGE(PG8_SB(1, 1), b3 + hstepB, voffB); PG8_STAGE_A(PG8_SA(1, 0), a3, 0, last);
;             PG8_WAIT_V(8); PG8_WAIT_L(0); PG8_BAR; PG8_MMA(1, 0, At, B0); PG8_MMA(1, 1, At, B1); PG8_BAR; PG8_SCHED;
;             } else {
;             PG8_LDB(B0, 0, 0); PG8_SCHED; PG8_LDA(At, 0, 0); PG8_STAGE(PG8_SA(1, 1), a1 + hstep, voffA);
;             PG8_WAIT_L(8); PG8_BAR; PG8_WAIT_L(0); PG8_MMA(0, 0, At, B0); PG8_BAR; PG8_SCHED;
;             PG8_LDB(B1, 0, 1); PG8_STAGE(PG8_SB(0, 0), b2, voffB);
;             PG8_BAR; PG8_WAIT_L(0); PG8_MMA(0, 1, At, B1); PG8_BAR;
;             PG8_LDA(At, 0, 1); PG8_STAGE(PG8_SA(0, 0), a2, voffA);
;             PG8_BAR; PG8_WAIT_L(0); PG8_MMA(1, 0, At, B0); PG8_BAR; PG8_SCHED;
;             PG8_STAGE(PG8_SB(0, 1), b2 + hstepB, voffB);
;             PG8_WAIT_V(6); PG8_BAR; PG8_MMA(1, 1, At, B1); PG8_BAR;
;             PG8_LDB(B0, 1, 0); PG8_SCHED; PG8_LDA(At, 1, 0); PG8_STAGE(PG8_SA(0, 1), a2 + hstep, voffA);
;             PG8_WAIT_L(8); PG8_BAR; PG8_WAIT_L(0); PG8_MMA(0, 0, At, B0); PG8_BAR; PG8_SCHED;
;             PG8_LDB(B1, 1, 1); PG8_STAGE(PG8_SB(1, 0), b3, voffB);
;             PG8_BAR; PG8_WAIT_L(0); PG8_MMA(0, 1, At, B1); PG8_BAR;
;             PG8_LDA(At, 1, 1); PG8_STAGE(PG8_SA(1, 0), a3, voffA);
;             PG8_BAR; PG8_WAIT_L(0); PG8_MMA(1, 0, At, B0); PG8_BAR; PG8_SCHED;
;             PG8_STAGE(PG8_SB(1, 1), b3 + hstepB, voffB);
;             PG8_WAIT_V(6); PG8_BAR; PG8_MMA(1, 1, At, B1); PG8_BAR;
;             }
;         }
;         if constexpr (F8) asm volatile("s_nop 15\n\ts_nop 15\n\ts_nop 15" ::: "memory");
;         if constexpr (ALIGN_EPI) { if (wr == 0) PG8_BAR; }
	s_add_i32 s48, 0, 0x18000
	s_add_i32 s49, 0, 0x1c000
	v_add_u32_e32 v14, s48, v186
	v_add_u32_e32 v30, s49, v186
	ds_read_b128 v[2:5], v14
	ds_read_b128 v[6:9], v14 offset:1024
	ds_read_b128 v[10:13], v14 offset:2048
	ds_read_b128 v[14:17], v14 offset:3072
	ds_read_b128 v[18:21], v30
	ds_read_b128 v[22:25], v30 offset:1024
	ds_read_b128 v[26:29], v30 offset:2048
	ds_read_b128 v[30:33], v30 offset:3072
	s_add_u32 s26, s26, 0x40000
	s_addc_u32 s27, s27, 0
	s_mov_b32 m0, s31
	v_lshl_add_u64 v[226:227], s[26:27], 0, v[168:169]
	ds_read_b128 v[194:197], v190 offset:32768
	ds_read_b128 v[198:201], v190 offset:33792
	ds_read_b128 v[202:205], v190 offset:34816
	ds_read_b128 v[206:209], v190 offset:35840
	ds_read_b128 v[210:213], v190 offset:36864
	ds_read_b128 v[214:217], v190 offset:37888
	ds_read_b128 v[218:221], v190 offset:38912
	ds_read_b128 v[222:225], v190 offset:39936
	global_load_lds_dwordx4 v[226:227], off
	v_lshl_add_u64 v[226:227], s[26:27], 0, v[164:165]
	s_mov_b32 m0, s34
	s_nop 0
	global_load_lds_dwordx4 v[226:227], off
	s_waitcnt vmcnt(8)
	s_waitcnt lgkmcnt(0)
	s_barrier
	s_setprio 1
	s_nop 3
	s_waitcnt lgkmcnt(0)
	v_mfma_scale_f32_16x16x128_f8f6f4 v[158:161], v[2:9], v[194:201], v[158:161], v191, v192 op_sel_hi:[0,0,0]
	v_mfma_scale_f32_16x16x128_f8f6f4 v[154:157], v[10:17], v[194:201], v[154:157], v191, v192 op_sel_hi:[0,0,0]
	v_mfma_scale_f32_16x16x128_f8f6f4 v[142:145], v[2:9], v[202:209], v[142:145], v191, v192 op_sel_hi:[0,0,0]
	v_mfma_scale_f32_16x16x128_f8f6f4 v[138:141], v[10:17], v[202:209], v[138:141], v191, v192 op_sel_hi:[0,0,0]
	v_mfma_scale_f32_16x16x128_f8f6f4 v[126:129], v[2:9], v[210:217], v[126:129], v191, v192 op_sel_hi:[0,0,0]
	v_mfma_scale_f32_16x16x128_f8f6f4 v[122:125], v[10:17], v[210:217], v[122:125], v191, v192 op_sel_hi:[0,0,0]
	v_mfma_scale_f32_16x16x128_f8f6f4 v[110:113], v[2:9], v[218:225], v[110:113], v191, v192 op_sel_hi:[0,0,0]
	v_mfma_scale_f32_16x16x128_f8f6f4 v[106:109], v[10:17], v[218:225], v[106:109], v191, v192 op_sel_hi:[0,0,0]
	s_setprio 0
	s_setprio 1
	s_nop 3
	v_mfma_scale_f32_16x16x128_f8f6f4 v[150:153], v[18:25], v[194:201], v[150:153], v191, v192 op_sel_hi:[0,0,0]
	v_mfma_scale_f32_16x16x128_f8f6f4 v[146:149], v[26:33], v[194:201], v[146:149], v191, v192 op_sel_hi:[0,0,0]
	v_mfma_scale_f32_16x16x128_f8f6f4 v[134:137], v[18:25], v[202:209], v[134:137], v191, v192 op_sel_hi:[0,0,0]
	v_mfma_scale_f32_16x16x128_f8f6f4 v[130:133], v[26:33], v[202:209], v[130:133], v191, v192 op_sel_hi:[0,0,0]
	v_mfma_scale_f32_16x16x128_f8f6f4 v[118:121], v[18:25], v[210:217], v[118:121], v191, v192 op_sel_hi:[0,0,0]
	v_mfma_scale_f32_16x16x128_f8f6f4 v[114:117], v[26:33], v[210:217], v[114:117], v191, v192 op_sel_hi:[0,0,0]
	v_mfma_scale_f32_16x16x128_f8f6f4 v[102:105], v[18:25], v[218:225], v[102:105], v191, v192 op_sel_hi:[0,0,0]
	v_mfma_scale_f32_16x16x128_f8f6f4 v[98:101], v[26:33], v[218:225], v[98:101], v191, v192 op_sel_hi:[0,0,0]
	s_setprio 0
	s_barrier
	s_add_i32 s26, s48, s28
	v_lshl_add_u64 v[178:179], v[178:179], 0, s[8:9]
	s_mov_b32 m0, s26
	ds_read_b128 v[194:197], v190 offset:49152
	ds_read_b128 v[198:201], v190 offset:50176
	ds_read_b128 v[202:205], v190 offset:51200
	ds_read_b128 v[206:209], v190 offset:52224
	ds_read_b128 v[210:213], v190 offset:53248
	ds_read_b128 v[214:217], v190 offset:54272
	ds_read_b128 v[218:221], v190 offset:55296
	ds_read_b128 v[222:225], v190 offset:56320
	global_load_lds_dwordx4 v[178:179], off
	s_add_i32 m0, s26, 0x2000
	s_add_u32 s24, s24, 0x4080
	v_lshl_add_u64 v[178:179], v[180:181], 0, s[8:9]
	s_addc_u32 s25, s25, 0
	s_add_i32 s26, s49, s28
	global_load_lds_dwordx4 v[178:179], off
	v_lshl_add_u64 v[178:179], s[24:25], 0, v[166:167]
	s_mov_b32 m0, s26
	s_nop 0
	global_load_lds_dwordx4 v[178:179], off
	v_lshl_add_u64 v[178:179], s[24:25], 0, v[162:163]
	s_add_i32 m0, s26, 0x2000
	s_nop 0
	global_load_lds_dwordx4 v[178:179], off
	v_lshl_add_u64 v[178:179], v[182:183], 0, s[8:9]
	s_mov_b32 m0, s38
	s_nop 0
	global_load_lds_dwordx4 v[178:179], off
	v_lshl_add_u64 v[178:179], v[184:185], 0, s[8:9]
	s_mov_b32 m0, s39
	s_nop 0
	global_load_lds_dwordx4 v[178:179], off
	s_waitcnt vmcnt(8)
	s_waitcnt lgkmcnt(0)
	s_barrier
	s_setprio 1
	s_nop 3
	s_waitcnt lgkmcnt(0)
	v_mfma_scale_f32_16x16x128_f8f6f4 v[94:97], v[2:9], v[194:201], v[94:97], v191, v192 op_sel_hi:[0,0,0]
	v_mfma_scale_f32_16x16x128_f8f6f4 v[90:93], v[10:17], v[194:201], v[90:93], v191, v192 op_sel_hi:[0,0,0]
	v_mfma_scale_f32_16x16x128_f8f6f4 v[78:81], v[2:9], v[202:209], v[78:81], v191, v192 op_sel_hi:[0,0,0]
	v_mfma_scale_f32_16x16x128_f8f6f4 v[74:77], v[10:17], v[202:209], v[74:77], v191, v192 op_sel_hi:[0,0,0]
	v_mfma_scale_f32_16x16x128_f8f6f4 v[62:65], v[2:9], v[210:217], v[62:65], v191, v192 op_sel_hi:[0,0,0]
	v_mfma_scale_f32_16x16x128_f8f6f4 v[58:61], v[10:17], v[210:217], v[58:61], v191, v192 op_sel_hi:[0,0,0]
	v_mfma_scale_f32_16x16x128_f8f6f4 v[46:49], v[2:9], v[218:225], v[46:49], v191, v192 op_sel_hi:[0,0,0]
	v_mfma_scale_f32_16x16x128_f8f6f4 v[42:45], v[10:17], v[218:225], v[42:45], v191, v192 op_sel_hi:[0,0,0]
	s_setprio 0
	s_setprio 1
	s_nop 3
	v_mfma_scale_f32_16x16x128_f8f6f4 v[86:89], v[18:25], v[194:201], v[86:89], v191, v192 op_sel_hi:[0,0,0]
	v_mfma_scale_f32_16x16x128_f8f6f4 v[82:85], v[26:33], v[194:201], v[82:85], v191, v192 op_sel_hi:[0,0,0]
	v_mfma_scale_f32_16x16x128_f8f6f4 v[70:73], v[18:25], v[202:209], v[70:73], v191, v192 op_sel_hi:[0,0,0]
	v_mfma_scale_f32_16x16x128_f8f6f4 v[66:69], v[26:33], v[202:209], v[66:69], v191, v192 op_sel_hi:[0,0,0]
	v_mfma_scale_f32_16x16x128_f8f6f4 v[54:57], v[18:25], v[210:217], v[54:57], v191, v192 op_sel_hi:[0,0,0]
	v_mfma_scale_f32_16x16x128_f8f6f4 v[50:53], v[26:33], v[210:217], v[50:53], v191, v192 op_sel_hi:[0,0,0]
	v_mfma_scale_f32_16x16x128_f8f6f4 v[38:41], v[18:25], v[218:225], v[38:41], v191, v192 op_sel_hi:[0,0,0]
	v_mfma_scale_f32_16x16x128_f8f6f4 v[34:37], v[26:33], v[218:225], v[34:37], v191, v192 op_sel_hi:[0,0,0]
	s_setprio 0
	s_barrier
	s_add_i32 s47, s47, 2
	s_add_u32 s22, s22, 0x100
	s_addc_u32 s23, s23, 0
	s_add_u32 s45, s45, 0x100
	s_addc_u32 s46, s46, 0
	s_cmp_gt_u32 s47, 13
	s_cbranch_scc0 .LBB0_895
	s_and_b64 vcc, exec, s[10:11]
	s_cbranch_vccz .LBB0_898
	s_barrier
; __device__ __forceinline__ unsigned pk4_fp8(float a, float b, float c, float d) { unsigned w = 0u; w = __builtin_amdgcn_cvt_pk_fp8_f32(a, b, w, false); w = __builtin_amdgcn_cvt_pk_fp8_f32(c, d, w, true); return w; }
; __device__ __forceinline__ float clamp448(float v) { return __builtin_amdgcn_fmed3f(v, -448.f, 448.f); }
;     __device__ __forceinline__ void operator()(const f32x4 (&acc)[2][2][4][2], const Unit& u, int wr, int wc, int fr, int fq) const {
;         const int row0 = u.pm * BM + wr * 64 + fr, col0 = u.pn * BM + wc * 64 + 16 * fq;
; #pragma unroll
;         for (int ai = 0; ai < 2; ++ai)
; #pragma unroll
;             for (int m = 0; m < 4; ++m) { const int row = row0 + ai * HALF + m * 16; const float gt = gate[row] * YSCALE; unsigned char* rowp = O + (size_t)row * ldc + col0;
;                 unsigned w[4];
; #pragma unroll
;                 for (int bj = 0; bj < 2; ++bj)
; #pragma unroll
;                     for (int n = 0; n < 2; ++n) { const f32x4 v = acc[ai][bj][m][n] * gt; w[2 * bj + n] = pk4_fp8(clamp448(v[0]), clamp448(v[1]), clamp448(v[2]), clamp448(v[3])); }
;                 *(u32x4*)rowp = (u32x4){w[0], w[1], w[2], w[3]}; }
.LBB0_898:
	v_lshl_add_u32 v2, s20, 8, v1
	v_ashrrev_i32_e32 v3, 31, v2
	v_lshl_add_u64 v[6:7], v[2:3], 2, s[0:1]
	global_load_dword v228, v[6:7], off
	global_load_dword v229, v[6:7], off offset:64
	global_load_dword v230, v[6:7], off offset:128
	global_load_dword v231, v[6:7], off offset:192
	global_load_dword v232, v[6:7], off offset:512
	global_load_dword v233, v[6:7], off offset:576
	global_load_dword v234, v[6:7], off offset:640
	global_load_dword v235, v[6:7], off offset:704
	v_lshlrev_b64 v[8:9], 10, v[2:3]
	v_lshl_or_b32 v10, s33, 8, v187
	v_ashrrev_i32_e32 v11, 31, v10
	v_lshl_add_u64 v[8:9], s[94:95], 0, v[8:9]
	v_lshl_add_u64 v[8:9], v[8:9], 0, v[10:11]
	s_mov_b32 s13, 0x20000
	s_mov_b64 s[20:21], -1
	s_waitcnt vmcnt(0)
	v_mul_f32_e32 v4, 0x42000000, v228
	v_pk_mul_f32 v[12:13], v[160:161], v[4:5] op_sel_hi:[1,0]
	v_pk_mul_f32 v[14:15], v[158:159], v[4:5] op_sel_hi:[1,0]
	v_med3_f32 v13, v13, s42, v193
	v_med3_f32 v3, v14, s42, v193
	v_med3_f32 v5, v15, s42, v193
	v_med3_f32 v14, v12, s42, v193
	v_mov_b32_e32 v12, 0
	v_cvt_pk_fp8_f32 v12, v3, v5
	v_pk_mul_f32 v[16:17], v[154:155], v[4:5] op_sel_hi:[1,0]
	v_cvt_pk_fp8_f32 v12, v14, v13 op_sel:[0,0,1]
	v_pk_mul_f32 v[14:15], v[156:157], v[4:5] op_sel_hi:[1,0]
	v_med3_f32 v3, v16, s42, v193
	v_med3_f32 v5, v17, s42, v193
	v_mov_b32_e32 v13, 0
	v_cvt_pk_fp8_f32 v13, v3, v5
	v_med3_f32 v14, v14, s42, v193
	v_med3_f32 v15, v15, s42, v193
	v_pk_mul_f32 v[16:17], v[150:151], v[4:5] op_sel_hi:[1,0]
	v_cvt_pk_fp8_f32 v13, v14, v15 op_sel:[0,0,1]
	v_pk_mul_f32 v[14:15], v[152:153], v[4:5] op_sel_hi:[1,0]
	v_med3_f32 v3, v16, s42, v193
	v_med3_f32 v5, v17, s42, v193
	v_med3_f32 v16, v14, s42, v193
	v_mov_b32_e32 v14, 0
	v_cvt_pk_fp8_f32 v14, v3, v5
	v_med3_f32 v15, v15, s42, v193
	v_cvt_pk_fp8_f32 v14, v16, v15 op_sel:[0,0,1]
	v_pk_mul_f32 v[16:17], v[148:149], v[4:5] op_sel_hi:[1,0]
	v_pk_mul_f32 v[4:5], v[146:147], v[4:5] op_sel_hi:[1,0]
	v_mov_b32_e32 v15, 0
	v_med3_f32 v3, v4, s42, v193
	v_med3_f32 v4, v5, s42, v193
	v_cvt_pk_fp8_f32 v15, v3, v4
	v_med3_f32 v5, v16, s42, v193
	v_med3_f32 v16, v17, s42, v193
	v_or_b32_e32 v4, 16, v2
	v_cvt_pk_fp8_f32 v15, v5, v16 op_sel:[0,0,1]
	v_ashrrev_i32_e32 v5, 31, v4
	global_store_dwordx4 v[8:9], v[12:15], off
	s_nop 1
	v_lshl_add_u64 v[12:13], v[4:5], 2, s[0:1]
	s_nop 1
	v_lshlrev_b64 v[4:5], 10, v[4:5]
	v_lshl_add_u64 v[4:5], s[94:95], 0, v[4:5]
	v_lshl_add_u64 v[4:5], v[4:5], 0, v[10:11]
	v_mul_f32_e32 v16, 0x42000000, v229
	v_pk_mul_f32 v[12:13], v[144:145], v[16:17] op_sel_hi:[1,0]
	v_pk_mul_f32 v[14:15], v[142:143], v[16:17] op_sel_hi:[1,0]
	v_med3_f32 v13, v13, s42, v193
	v_med3_f32 v3, v14, s42, v193
	v_med3_f32 v14, v15, s42, v193
	v_med3_f32 v15, v12, s42, v193
	v_mov_b32_e32 v12, 0
	v_cvt_pk_fp8_f32 v12, v3, v14
	v_pk_mul_f32 v[18:19], v[138:139], v[16:17] op_sel_hi:[1,0]
	v_cvt_pk_fp8_f32 v12, v15, v13 op_sel:[0,0,1]
	v_pk_mul_f32 v[14:15], v[140:141], v[16:17] op_sel_hi:[1,0]
	v_med3_f32 v3, v18, s42, v193
	v_med3_f32 v17, v19, s42, v193
	v_mov_b32_e32 v13, 0
	v_cvt_pk_fp8_f32 v13, v3, v17
	v_med3_f32 v14, v14, s42, v193
	v_med3_f32 v15, v15, s42, v193
	v_pk_mul_f32 v[18:19], v[134:135], v[16:17] op_sel_hi:[1,0]
	v_cvt_pk_fp8_f32 v13, v14, v15 op_sel:[0,0,1]
	v_pk_mul_f32 v[14:15], v[136:137], v[16:17] op_sel_hi:[1,0]
	v_med3_f32 v3, v18, s42, v193
	v_med3_f32 v17, v19, s42, v193
	v_med3_f32 v18, v14, s42, v193
	v_mov_b32_e32 v14, 0
	v_cvt_pk_fp8_f32 v14, v3, v17
	v_med3_f32 v15, v15, s42, v193
	v_cvt_pk_fp8_f32 v14, v18, v15 op_sel:[0,0,1]
	v_pk_mul_f32 v[18:19], v[132:133], v[16:17] op_sel_hi:[1,0]
	v_pk_mul_f32 v[16:17], v[130:131], v[16:17] op_sel_hi:[1,0]
	v_mov_b32_e32 v15, 0
	v_med3_f32 v3, v16, s42, v193
	v_med3_f32 v16, v17, s42, v193
	v_cvt_pk_fp8_f32 v15, v3, v16
	v_med3_f32 v17, v18, s42, v193
	v_med3_f32 v18, v19, s42, v193
	v_cvt_pk_fp8_f32 v15, v17, v18 op_sel:[0,0,1]
	global_store_dwordx4 v[4:5], v[12:15], off
	v_or_b32_e32 v4, 32, v2
	v_ashrrev_i32_e32 v5, 31, v4
	v_lshl_add_u64 v[12:13], v[4:5], 2, s[0:1]
	s_nop 1
	v_lshlrev_b64 v[4:5], 10, v[4:5]
	v_lshl_add_u64 v[4:5], s[94:95], 0, v[4:5]
	v_or_b32_e32 v2, 48, v2
	v_lshl_add_u64 v[4:5], v[4:5], 0, v[10:11]
	v_mul_f32_e32 v16, 0x42000000, v230
	v_pk_mul_f32 v[12:13], v[128:129], v[16:17] op_sel_hi:[1,0]
	v_pk_mul_f32 v[14:15], v[126:127], v[16:17] op_sel_hi:[1,0]
	v_med3_f32 v13, v13, s42, v193
	v_med3_f32 v3, v14, s42, v193
	v_med3_f32 v14, v15, s42, v193
	v_med3_f32 v15, v12, s42, v193
	v_mov_b32_e32 v12, 0
	v_cvt_pk_fp8_f32 v12, v3, v14
	v_pk_mul_f32 v[18:19], v[122:123], v[16:17] op_sel_hi:[1,0]
	v_cvt_pk_fp8_f32 v12, v15, v13 op_sel:[0,0,1]
	v_pk_mul_f32 v[14:15], v[124:125], v[16:17] op_sel_hi:[1,0]
	v_med3_f32 v3, v18, s42, v193
	v_med3_f32 v17, v19, s42, v193
	v_mov_b32_e32 v13, 0
	v_cvt_pk_fp8_f32 v13, v3, v17
	v_med3_f32 v14, v14, s42, v193
	v_med3_f32 v15, v15, s42, v193
	v_pk_mul_f32 v[18:19], v[118:119], v[16:17] op_sel_hi:[1,0]
	v_cvt_pk_fp8_f32 v13, v14, v15 op_sel:[0,0,1]
	v_pk_mul_f32 v[14:15], v[120:121], v[16:17] op_sel_hi:[1,0]
	v_med3_f32 v3, v18, s42, v193
	v_med3_f32 v17, v19, s42, v193
	v_med3_f32 v18, v14, s42, v193
	v_mov_b32_e32 v14, 0
	v_cvt_pk_fp8_f32 v14, v3, v17
	v_med3_f32 v15, v15, s42, v193
	v_cvt_pk_fp8_f32 v14, v18, v15 op_sel:[0,0,1]
	v_pk_mul_f32 v[18:19], v[116:117], v[16:17] op_sel_hi:[1,0]
	v_pk_mul_f32 v[16:17], v[114:115], v[16:17] op_sel_hi:[1,0]
	v_mov_b32_e32 v15, 0
	v_med3_f32 v3, v16, s42, v193
	v_med3_f32 v16, v17, s42, v193
	v_cvt_pk_fp8_f32 v15, v3, v16
	v_med3_f32 v17, v18, s42, v193
	v_med3_f32 v18, v19, s42, v193
	v_ashrrev_i32_e32 v3, 31, v2
	v_cvt_pk_fp8_f32 v15, v17, v18 op_sel:[0,0,1]
; __device__ __forceinline__ unsigned pk4_fp8(float a, float b, float c, float d) { unsigned w = 0u; w = __builtin_amdgcn_cvt_pk_fp8_f32(a, b, w, false); w = __builtin_amdgcn_cvt_pk_fp8_f32(c, d, w, true); return w; }
; __device__ __forceinline__ float clamp448(float v) { return __builtin_amdgcn_fmed3f(v, -448.f, 448.f); }
;     __device__ __forceinline__ void operator()(const f32x4 (&acc)[2][2][4][2], const Unit& u, int wr, int wc, int fr, int fq) const {
;     ...
;             for (int m = 0; m < 4; ++m) { const int row = row0 + ai * HALF + m * 16; const float gt = gate[row] * YSCALE; unsigned char* rowp = O + (size_t)row * ldc + col0;
;                 unsigned w[4];
; #pragma unroll
;                 for (int bj = 0; bj < 2; ++bj)
; #pragma unroll
;                     for (int n = 0; n < 2; ++n) { const f32x4 v = acc[ai][bj][m][n] * gt; w[2 * bj + n] = pk4_fp8(clamp448(v[0]), clamp448(v[1]), clamp448(v[2]), clamp448(v[3])); }
;                 *(u32x4*)rowp = (u32x4){w[0], w[1], w[2], w[3]}; }
	global_store_dwordx4 v[4:5], v[12:15], off
	v_lshl_add_u64 v[4:5], v[2:3], 2, s[0:1]
	s_nop 1
	v_lshlrev_b64 v[2:3], 10, v[2:3]
	v_lshl_add_u64 v[12:13], s[94:95], 0, v[2:3]
	v_lshl_add_u64 v[10:11], v[12:13], 0, v[10:11]
	v_mul_f32_e32 v14, 0x42000000, v231
	v_pk_mul_f32 v[2:3], v[112:113], v[14:15] op_sel_hi:[1,0]
	v_pk_mul_f32 v[4:5], v[110:111], v[14:15] op_sel_hi:[1,0]
	v_med3_f32 v15, v2, s42, v193
	v_med3_f32 v4, v4, s42, v193
	v_med3_f32 v5, v5, s42, v193
	v_mov_b32_e32 v2, 0
	v_cvt_pk_fp8_f32 v2, v4, v5
	v_med3_f32 v3, v3, s42, v193
	v_pk_mul_f32 v[16:17], v[106:107], v[14:15] op_sel_hi:[1,0]
	v_pk_mul_f32 v[4:5], v[108:109], v[14:15] op_sel_hi:[1,0]
	v_cvt_pk_fp8_f32 v2, v15, v3 op_sel:[0,0,1]
	v_med3_f32 v15, v16, s42, v193
	v_med3_f32 v16, v17, s42, v193
	v_mov_b32_e32 v3, 0
	v_cvt_pk_fp8_f32 v3, v15, v16
	v_med3_f32 v4, v4, s42, v193
	v_med3_f32 v5, v5, s42, v193
	v_pk_mul_f32 v[16:17], v[102:103], v[14:15] op_sel_hi:[1,0]
	v_cvt_pk_fp8_f32 v3, v4, v5 op_sel:[0,0,1]
	v_pk_mul_f32 v[4:5], v[104:105], v[14:15] op_sel_hi:[1,0]
	v_med3_f32 v15, v16, s42, v193
	v_med3_f32 v16, v17, s42, v193
	v_med3_f32 v17, v4, s42, v193
	v_mov_b32_e32 v4, 0
	v_cvt_pk_fp8_f32 v4, v15, v16
	v_med3_f32 v5, v5, s42, v193
	v_cvt_pk_fp8_f32 v4, v17, v5 op_sel:[0,0,1]
	v_pk_mul_f32 v[16:17], v[100:101], v[14:15] op_sel_hi:[1,0]
	v_pk_mul_f32 v[14:15], v[98:99], v[14:15] op_sel_hi:[1,0]
	v_mov_b32_e32 v5, 0
	v_med3_f32 v14, v14, s42, v193
	v_med3_f32 v15, v15, s42, v193
	v_cvt_pk_fp8_f32 v5, v14, v15
	v_med3_f32 v16, v16, s42, v193
	v_med3_f32 v17, v17, s42, v193
	v_cvt_pk_fp8_f32 v5, v16, v17 op_sel:[0,0,1]
	global_store_dwordx4 v[10:11], v[2:5], off
	s_nop 1
	v_mul_f32_e32 v10, 0x42000000, v232
	v_pk_mul_f32 v[2:3], v[96:97], v[10:11] op_sel_hi:[1,0]
	v_pk_mul_f32 v[4:5], v[94:95], v[10:11] op_sel_hi:[1,0]
	v_med3_f32 v11, v2, s42, v193
	v_med3_f32 v4, v4, s42, v193
	v_med3_f32 v5, v5, s42, v193
	v_mov_b32_e32 v2, 0
	v_cvt_pk_fp8_f32 v2, v4, v5
	v_med3_f32 v3, v3, s42, v193
	v_pk_mul_f32 v[12:13], v[90:91], v[10:11] op_sel_hi:[1,0]
	v_pk_mul_f32 v[4:5], v[92:93], v[10:11] op_sel_hi:[1,0]
	v_cvt_pk_fp8_f32 v2, v11, v3 op_sel:[0,0,1]
	v_med3_f32 v11, v12, s42, v193
	v_med3_f32 v12, v13, s42, v193
	v_mov_b32_e32 v3, 0
	v_cvt_pk_fp8_f32 v3, v11, v12
	v_med3_f32 v4, v4, s42, v193
	v_med3_f32 v5, v5, s42, v193
	v_pk_mul_f32 v[12:13], v[86:87], v[10:11] op_sel_hi:[1,0]
	v_cvt_pk_fp8_f32 v3, v4, v5 op_sel:[0,0,1]
	v_pk_mul_f32 v[4:5], v[88:89], v[10:11] op_sel_hi:[1,0]
	v_med3_f32 v11, v12, s42, v193
	v_med3_f32 v12, v13, s42, v193
	v_med3_f32 v13, v4, s42, v193
	v_mov_b32_e32 v4, 0
	v_cvt_pk_fp8_f32 v4, v11, v12
	v_med3_f32 v5, v5, s42, v193
	v_cvt_pk_fp8_f32 v4, v13, v5 op_sel:[0,0,1]
	v_pk_mul_f32 v[12:13], v[84:85], v[10:11] op_sel_hi:[1,0]
	v_pk_mul_f32 v[10:11], v[82:83], v[10:11] op_sel_hi:[1,0]
	v_mov_b32_e32 v5, 0
	v_med3_f32 v10, v10, s42, v193
	v_med3_f32 v11, v11, s42, v193
	v_cvt_pk_fp8_f32 v5, v10, v11
	v_med3_f32 v12, v12, s42, v193
	v_med3_f32 v13, v13, s42, v193
	v_add_co_u32_e32 v10, vcc, s13, v8
	v_cvt_pk_fp8_f32 v5, v12, v13 op_sel:[0,0,1]
	s_nop 0
	v_addc_co_u32_e32 v11, vcc, 0, v9, vcc
	s_mov_b32 s13, 0x24000
	global_store_dwordx4 v[10:11], v[2:5], off
	s_nop 1
	v_mul_f32_e32 v10, 0x42000000, v233
	v_pk_mul_f32 v[2:3], v[80:81], v[10:11] op_sel_hi:[1,0]
	v_pk_mul_f32 v[4:5], v[78:79], v[10:11] op_sel_hi:[1,0]
	v_med3_f32 v11, v2, s42, v193
	v_med3_f32 v4, v4, s42, v193
	v_med3_f32 v5, v5, s42, v193
	v_mov_b32_e32 v2, 0
	v_cvt_pk_fp8_f32 v2, v4, v5
	v_med3_f32 v3, v3, s42, v193
	v_pk_mul_f32 v[12:13], v[74:75], v[10:11] op_sel_hi:[1,0]
	v_pk_mul_f32 v[4:5], v[76:77], v[10:11] op_sel_hi:[1,0]
	v_cvt_pk_fp8_f32 v2, v11, v3 op_sel:[0,0,1]
	v_med3_f32 v11, v12, s42, v193
	v_med3_f32 v12, v13, s42, v193
	v_mov_b32_e32 v3, 0
	v_cvt_pk_fp8_f32 v3, v11, v12
	v_med3_f32 v4, v4, s42, v193
	v_med3_f32 v5, v5, s42, v193
	v_pk_mul_f32 v[12:13], v[70:71], v[10:11] op_sel_hi:[1,0]
; #define PG8_BAR __builtin_amdgcn_s_barrier()
; __device__ __forceinline__ unsigned pk4_fp8(float a, float b, float c, float d) { unsigned w = 0u; w = __builtin_amdgcn_cvt_pk_fp8_f32(a, b, w, false); w = __builtin_amdgcn_cvt_pk_fp8_f32(c, d, w, true); return w; }
; __device__ __forceinline__ float clamp448(float v) { return __builtin_amdgcn_fmed3f(v, -448.f, 448.f); }
;     ...
;         if (!has_next) break;
; #pragma unroll
;         for (int a = 0; a < 2; ++a)
; #pragma unroll
;             for (int b = 0; b < 2; ++b)
; #pragma unroll
;                 for (int m = 0; m < 4; ++m)
; #pragma unroll
;                     for (int n = 0; n < 2; ++n) acc[a][b][m][n] = (f32x4){0.f, 0.f, 0.f, 0.f};
;         cur = nxt; cA = nA; cB = nB; ++ui;
;         if constexpr (Sched::GATHER) { _Pragma("unroll") for (int h_ = 0; h_ < 2; ++h_) _Pragma("unroll") for (int i_ = 0; i_ < 2; ++i_) vA[h_][i_] = vAn[h_][i_]; }
;         if constexpr (ALIGN_EPI) { if (wr == 1) PG8_BAR; }
;     __device__ __forceinline__ void operator()(const f32x4 (&acc)[2][2][4][2], const Unit& u, int wr, int wc, int fr, int fq) const {
;     ...
;             for (int m = 0; m < 4; ++m) { const int row = row0 + ai * HALF + m * 16; const float gt = gate[row] * YSCALE; unsigned char* rowp = O + (size_t)row * ldc + col0;
;                 unsigned w[4];
; #pragma unroll
;                 for (int bj = 0; bj < 2; ++bj)
; #pragma unroll
;                     for (int n = 0; n < 2; ++n) { const f32x4 v = acc[ai][bj][m][n] * gt; w[2 * bj + n] = pk4_fp8(clamp448(v[0]), clamp448(v[1]), clamp448(v[2]), clamp448(v[3])); }
;                 *(u32x4*)rowp = (u32x4){w[0], w[1], w[2], w[3]}; }
	v_cvt_pk_fp8_f32 v3, v4, v5 op_sel:[0,0,1]
	v_pk_mul_f32 v[4:5], v[72:73], v[10:11] op_sel_hi:[1,0]
	v_med3_f32 v11, v12, s42, v193
	v_med3_f32 v12, v13, s42, v193
	v_med3_f32 v13, v4, s42, v193
	v_mov_b32_e32 v4, 0
	v_cvt_pk_fp8_f32 v4, v11, v12
	v_med3_f32 v5, v5, s42, v193
	v_cvt_pk_fp8_f32 v4, v13, v5 op_sel:[0,0,1]
	v_pk_mul_f32 v[12:13], v[68:69], v[10:11] op_sel_hi:[1,0]
	v_pk_mul_f32 v[10:11], v[66:67], v[10:11] op_sel_hi:[1,0]
	v_mov_b32_e32 v5, 0
	v_med3_f32 v10, v10, s42, v193
	v_med3_f32 v11, v11, s42, v193
	v_cvt_pk_fp8_f32 v5, v10, v11
	v_med3_f32 v12, v12, s42, v193
	v_med3_f32 v13, v13, s42, v193
	v_add_co_u32_e32 v10, vcc, s13, v8
	v_cvt_pk_fp8_f32 v5, v12, v13 op_sel:[0,0,1]
	s_nop 0
	v_addc_co_u32_e32 v11, vcc, 0, v9, vcc
	s_mov_b32 s13, 0x28000
	global_store_dwordx4 v[10:11], v[2:5], off
	s_nop 1
	v_mul_f32_e32 v10, 0x42000000, v234
	v_pk_mul_f32 v[2:3], v[64:65], v[10:11] op_sel_hi:[1,0]
	v_pk_mul_f32 v[4:5], v[62:63], v[10:11] op_sel_hi:[1,0]
	v_med3_f32 v11, v2, s42, v193
	v_med3_f32 v4, v4, s42, v193
	v_med3_f32 v5, v5, s42, v193
	v_mov_b32_e32 v2, 0
	v_cvt_pk_fp8_f32 v2, v4, v5
	v_med3_f32 v3, v3, s42, v193
	v_pk_mul_f32 v[12:13], v[58:59], v[10:11] op_sel_hi:[1,0]
	v_pk_mul_f32 v[4:5], v[60:61], v[10:11] op_sel_hi:[1,0]
	v_cvt_pk_fp8_f32 v2, v11, v3 op_sel:[0,0,1]
	v_med3_f32 v11, v12, s42, v193
	v_med3_f32 v12, v13, s42, v193
	v_mov_b32_e32 v3, 0
	v_cvt_pk_fp8_f32 v3, v11, v12
	v_med3_f32 v4, v4, s42, v193
	v_med3_f32 v5, v5, s42, v193
	v_pk_mul_f32 v[12:13], v[54:55], v[10:11] op_sel_hi:[1,0]
	v_cvt_pk_fp8_f32 v3, v4, v5 op_sel:[0,0,1]
	v_pk_mul_f32 v[4:5], v[56:57], v[10:11] op_sel_hi:[1,0]
	v_med3_f32 v11, v12, s42, v193
	v_med3_f32 v12, v13, s42, v193
	v_med3_f32 v13, v4, s42, v193
	v_mov_b32_e32 v4, 0
	v_cvt_pk_fp8_f32 v4, v11, v12
	v_med3_f32 v5, v5, s42, v193
	v_cvt_pk_fp8_f32 v4, v13, v5 op_sel:[0,0,1]
	v_pk_mul_f32 v[12:13], v[52:53], v[10:11] op_sel_hi:[1,0]
	v_pk_mul_f32 v[10:11], v[50:51], v[10:11] op_sel_hi:[1,0]
	v_mov_b32_e32 v5, 0
	v_med3_f32 v10, v10, s42, v193
	v_med3_f32 v11, v11, s42, v193
	v_cvt_pk_fp8_f32 v5, v10, v11
	v_med3_f32 v12, v12, s42, v193
	v_med3_f32 v13, v13, s42, v193
	v_add_co_u32_e32 v10, vcc, s13, v8
	v_cvt_pk_fp8_f32 v5, v12, v13 op_sel:[0,0,1]
	s_nop 0
	v_addc_co_u32_e32 v11, vcc, 0, v9, vcc
	global_store_dwordx4 v[10:11], v[2:5], off
	s_nop 1
	v_mul_f32_e32 v6, 0x42000000, v235
	v_pk_mul_f32 v[2:3], v[48:49], v[6:7] op_sel_hi:[1,0]
	v_pk_mul_f32 v[4:5], v[46:47], v[6:7] op_sel_hi:[1,0]
	v_med3_f32 v7, v2, s42, v193
	v_med3_f32 v4, v4, s42, v193
	v_med3_f32 v5, v5, s42, v193
	v_mov_b32_e32 v2, 0
	v_cvt_pk_fp8_f32 v2, v4, v5
	v_med3_f32 v3, v3, s42, v193
	v_pk_mul_f32 v[10:11], v[42:43], v[6:7] op_sel_hi:[1,0]
	v_pk_mul_f32 v[4:5], v[44:45], v[6:7] op_sel_hi:[1,0]
	v_cvt_pk_fp8_f32 v2, v7, v3 op_sel:[0,0,1]
	v_med3_f32 v7, v10, s42, v193
	v_med3_f32 v10, v11, s42, v193
	v_mov_b32_e32 v3, 0
	v_cvt_pk_fp8_f32 v3, v7, v10
	v_med3_f32 v4, v4, s42, v193
	v_med3_f32 v5, v5, s42, v193
	v_pk_mul_f32 v[10:11], v[38:39], v[6:7] op_sel_hi:[1,0]
	v_cvt_pk_fp8_f32 v3, v4, v5 op_sel:[0,0,1]
	v_pk_mul_f32 v[4:5], v[40:41], v[6:7] op_sel_hi:[1,0]
	v_med3_f32 v7, v10, s42, v193
	v_med3_f32 v10, v11, s42, v193
	v_med3_f32 v11, v4, s42, v193
	v_mov_b32_e32 v4, 0
	v_cvt_pk_fp8_f32 v4, v7, v10
	v_med3_f32 v5, v5, s42, v193
	v_cvt_pk_fp8_f32 v4, v11, v5 op_sel:[0,0,1]
	v_pk_mul_f32 v[10:11], v[36:37], v[6:7] op_sel_hi:[1,0]
	v_pk_mul_f32 v[6:7], v[34:35], v[6:7] op_sel_hi:[1,0]
	v_mov_b32_e32 v5, 0
	v_med3_f32 v6, v6, s42, v193
	v_med3_f32 v7, v7, s42, v193
	v_cvt_pk_fp8_f32 v5, v6, v7
	v_med3_f32 v10, v10, s42, v193
	v_med3_f32 v11, v11, s42, v193
	v_add_co_u32_e32 v6, vcc, 0x2c000, v8
	v_cvt_pk_fp8_f32 v5, v10, v11 op_sel:[0,0,1]
	s_nop 0
	v_addc_co_u32_e32 v7, vcc, 0, v9, vcc
	s_andn2_b64 vcc, exec, s[2:3]
	global_store_dwordx4 v[6:7], v[2:5], off
	s_cbranch_vccnz .LBB0_891
	s_andn2_b64 vcc, exec, s[6:7]
	s_cbranch_vccnz .LBB0_890
	s_barrier
	s_branch .LBB0_890

; #define PG8_STAGE(bufoff, gbase, voff) do { _Pragma("unroll") for (int _i = 0; _i < 2; ++_i) \
;         __builtin_amdgcn_global_load_lds((const unsigned*)((const char*)(gbase) + (voff)[_i]), (PG8_LAS unsigned*)(lds + (bufoff) + ldsw + _i * 8192), 16, 0, 0); } while (0)
; #define PG8_STAGE_A(bufoff, gbase, h, nx) do { if constexpr (Sched::GATHER) { const unsigned vv_[2] = {(nx) ? vAn[h][0] : vA[h][0], (nx) ? vAn[h][1] : vA[h][1]}; PG8_STAGE(bufoff, gbase, vv_); } \
;         else { PG8_STAGE(bufoff, (gbase) + (h) * hstep, voffA); } } while (0)
; #define PG8_LDA(dst, b, h) do { _Pragma("unroll") for (int m = 0; m < 4; ++m) _Pragma("unroll") for (int k = 0; k < 2; ++k) dst[m][k] = *(const PG8_LAS bf16x8*)(lds + PG8_SA(b, h) + aoff + m * 2048 + k * 1024); } while (0)
; #define PG8_WAIT_V(n) asm volatile("s_waitcnt vmcnt(" #n ")" ::: "memory")
; #define PG8_WAIT_L(n) asm volatile("s_waitcnt lgkmcnt(" #n ")" ::: "memory")
;     ...
;         const bool has_next = S.next(ui + 1, nxt);
;         const char* nA = Sched::GATHER ? cA : (has_next ? (const char*)g.A + (size_t)nxt.pm * tstep : cA);
;         if constexpr (Sched::GATHER) { if (has_next) { PG8_AOFF(vAn, ui + 1); } else { _Pragma("unroll") for (int h_ = 0; h_ < 2; ++h_) _Pragma("unroll") for (int i_ = 0; i_ < 2; ++i_) vAn[h_][i_] = vA[h_][i_]; } } const char* nB = has_next ? (const char*)g.Bt + (size_t)nxt.pb * tstep : cB;
; #pragma nounroll
;         for (int t = 0; t < nt; t += 2) {
;             const bool last = (t == nt - 2);
;             const char* a1 = cA + (size_t)(t + 1) * kstep;
;             const char* a2 = last ? nA : cA + (size_t)(t + 2) * kstep; const char* b2 = last ? nB : cB + (size_t)(t + 2) * kstep;
;             const char* a3 = a2 + kstep; const char* b3 = b2 + kstep;
;             if (last && has_next) S.a_ready(nxt);
;             if constexpr (SP2) {
;             PG8_LDB(B0, 0, 0); PG8_LDB(B1, 0, 1); PG8_SCHED; PG8_LDA(At, 0, 0); PG8_STAGE_A(PG8_SA(1, 1), a1, 1, false);
;             PG8_WAIT_V(8); PG8_WAIT_L(0); PG8_BAR; PG8_MMA(0, 0, At, B0); PG8_MMA(0, 1, At, B1); PG8_BAR; PG8_SCHED;
;             PG8_LDA(At, 0, 1); PG8_STAGE(PG8_SB(0, 0), b2, voffB); PG8_STAGE(PG8_SB(0, 1), b2 + hstepB, voffB); PG8_STAGE_A(PG8_SA(0, 0), a2, 0, last);
;             PG8_WAIT_V(8); PG8_WAIT_L(0); PG8_BAR; PG8_MMA(1, 0, At, B0); PG8_MMA(1, 1, At, B1); PG8_BAR; PG8_SCHED;
.LBB0_1625:
	s_ashr_i32 s13, s12, 31
	s_lshl_b64 s[16:17], s[12:13], 19
	v_readlane_b32 s18, v255, 9
	v_readlane_b32 s19, v255, 10
	s_add_u32 s16, s18, s16
	s_addc_u32 s17, s19, s17
	s_and_b64 s[18:19], s[2:3], exec
	s_cselect_b32 s13, s17, s23
	s_cselect_b32 s46, s16, s22
	s_ashr_i32 s15, s14, 31
	s_lshl_b64 s[18:19], s[14:15], 19
	v_readlane_b32 s26, v255, 3
	v_readlane_b32 s27, v255, 4
	s_add_u32 s18, s26, s18
	s_addc_u32 s19, s27, s19
	s_and_b64 s[26:27], s[2:3], exec
	s_cselect_b32 s15, s19, s25
	s_cselect_b32 s47, s18, s24
	s_add_u32 s22, s22, 0x40080
	s_addc_u32 s23, s23, 0
	s_add_u32 s48, s24, 0x100
	s_addc_u32 s49, s25, 0
	s_mov_b32 s50, -2
	ds_read_b128 v[26:29], v188
	ds_read_b128 v[30:33], v188 offset:1024
	ds_read_b128 v[18:21], v188 offset:2048
	ds_read_b128 v[22:25], v188 offset:3072
	ds_read_b128 v[10:13], v189
	ds_read_b128 v[14:17], v189 offset:1024
	ds_read_b128 v[2:5], v189 offset:2048
	ds_read_b128 v[6:9], v189 offset:3072
	s_add_u32 s24, s22, 0xfffc0080
	s_addc_u32 s25, s23, -1
	s_cmp_eq_u32 s50, 12
	s_cselect_b32 s27, s13, s25
	s_cselect_b32 s26, s46, s24
	s_cselect_b32 s25, s15, s49
	s_cselect_b32 s24, s47, s48
	v_lshl_add_u64 v[218:219], s[22:23], 0, v[170:171]
	s_add_i32 m0, s28, 0xc000
	ds_read_b128 v[178:181], v190
	ds_read_b128 v[182:185], v190 offset:1024
	ds_read_b128 v[194:197], v190 offset:2048
	ds_read_b128 v[198:201], v190 offset:3072
	ds_read_b128 v[202:205], v190 offset:4096
	ds_read_b128 v[206:209], v190 offset:5120
	ds_read_b128 v[210:213], v190 offset:6144
	ds_read_b128 v[214:217], v190 offset:7168
	global_load_lds_dwordx4 v[218:219], off
	v_lshl_add_u64 v[218:219], s[22:23], 0, v[172:173]
	s_add_i32 m0, s28, 0xe000
	s_nop 0
	global_load_lds_dwordx4 v[218:219], off
	s_waitcnt vmcnt(8)
	s_waitcnt lgkmcnt(0)
	s_barrier
	s_setprio 1
	s_nop 3
	s_waitcnt lgkmcnt(0)
	v_mfma_scale_f32_16x16x128_f8f6f4 v[158:161], v[26:33], v[178:185], 0, v191, v192 op_sel_hi:[0,0,0]
	v_mfma_scale_f32_16x16x128_f8f6f4 v[154:157], v[18:25], v[178:185], 0, v191, v192 op_sel_hi:[0,0,0]
	v_mfma_scale_f32_16x16x128_f8f6f4 v[142:145], v[26:33], v[194:201], 0, v191, v192 op_sel_hi:[0,0,0]
	v_mfma_scale_f32_16x16x128_f8f6f4 v[138:141], v[18:25], v[194:201], 0, v191, v192 op_sel_hi:[0,0,0]
	v_mfma_scale_f32_16x16x128_f8f6f4 v[126:129], v[26:33], v[202:209], 0, v191, v192 op_sel_hi:[0,0,0]
	v_mfma_scale_f32_16x16x128_f8f6f4 v[122:125], v[18:25], v[202:209], 0, v191, v192 op_sel_hi:[0,0,0]
	v_mfma_scale_f32_16x16x128_f8f6f4 v[110:113], v[26:33], v[210:217], 0, v191, v192 op_sel_hi:[0,0,0]
	v_mfma_scale_f32_16x16x128_f8f6f4 v[106:109], v[18:25], v[210:217], 0, v191, v192 op_sel_hi:[0,0,0]
	s_setprio 0
	s_setprio 1
	s_nop 3
	v_mfma_scale_f32_16x16x128_f8f6f4 v[150:153], v[10:17], v[178:185], 0, v191, v192 op_sel_hi:[0,0,0]
	v_mfma_scale_f32_16x16x128_f8f6f4 v[146:149], v[2:9], v[178:185], 0, v191, v192 op_sel_hi:[0,0,0]
	v_mfma_scale_f32_16x16x128_f8f6f4 v[134:137], v[10:17], v[194:201], 0, v191, v192 op_sel_hi:[0,0,0]
	v_mfma_scale_f32_16x16x128_f8f6f4 v[130:133], v[2:9], v[194:201], 0, v191, v192 op_sel_hi:[0,0,0]
	v_mfma_scale_f32_16x16x128_f8f6f4 v[118:121], v[10:17], v[202:209], 0, v191, v192 op_sel_hi:[0,0,0]
	v_mfma_scale_f32_16x16x128_f8f6f4 v[114:117], v[2:9], v[202:209], 0, v191, v192 op_sel_hi:[0,0,0]
	v_mfma_scale_f32_16x16x128_f8f6f4 v[102:105], v[10:17], v[210:217], 0, v191, v192 op_sel_hi:[0,0,0]
	v_mfma_scale_f32_16x16x128_f8f6f4 v[98:101], v[2:9], v[210:217], 0, v191, v192 op_sel_hi:[0,0,0]
	s_setprio 0
	s_barrier
	s_add_i32 s51, s39, s21
	v_lshl_add_u64 v[178:179], s[24:25], 0, v[166:167]
	s_mov_b32 m0, s51
	ds_read_b128 v[194:197], v190 offset:16384
	ds_read_b128 v[198:201], v190 offset:17408
	ds_read_b128 v[202:205], v190 offset:18432
	ds_read_b128 v[206:209], v190 offset:19456
	ds_read_b128 v[210:213], v190 offset:20480
	ds_read_b128 v[214:217], v190 offset:21504
	ds_read_b128 v[218:221], v190 offset:22528
	ds_read_b128 v[222:225], v190 offset:23552
	global_load_lds_dwordx4 v[178:179], off
	s_add_i32 m0, s51, 0x2000
	s_add_u32 s52, s24, 0x4000
	v_lshl_add_u64 v[180:181], s[24:25], 0, v[162:163]
	s_addc_u32 s53, s25, 0
	s_add_i32 s51, s40, s21
	global_load_lds_dwordx4 v[180:181], off
	v_lshl_add_u64 v[182:183], s[52:53], 0, v[166:167]
	s_mov_b32 m0, s51
	v_lshl_add_u64 v[184:185], s[26:27], 0, v[164:165]
	global_load_lds_dwordx4 v[182:183], off
	v_lshl_add_u64 v[182:183], s[52:53], 0, v[162:163]
	s_add_i32 m0, s51, 0x2000
	s_nop 0
	global_load_lds_dwordx4 v[182:183], off
	v_lshl_add_u64 v[182:183], s[26:27], 0, v[168:169]
	s_mov_b32 m0, s28
	s_nop 0
	global_load_lds_dwordx4 v[182:183], off
	s_mov_b32 m0, s29
	s_nop 0
	global_load_lds_dwordx4 v[184:185], off
	s_waitcnt vmcnt(8)
	s_waitcnt lgkmcnt(0)
	s_barrier
	s_setprio 1
	s_nop 3
	s_waitcnt lgkmcnt(0)
	v_mfma_scale_f32_16x16x128_f8f6f4 v[94:97], v[26:33], v[194:201], 0, v191, v192 op_sel_hi:[0,0,0]
	v_mfma_scale_f32_16x16x128_f8f6f4 v[90:93], v[18:25], v[194:201], 0, v191, v192 op_sel_hi:[0,0,0]
	v_mfma_scale_f32_16x16x128_f8f6f4 v[78:81], v[26:33], v[202:209], 0, v191, v192 op_sel_hi:[0,0,0]
	v_mfma_scale_f32_16x16x128_f8f6f4 v[74:77], v[18:25], v[202:209], 0, v191, v192 op_sel_hi:[0,0,0]
	v_mfma_scale_f32_16x16x128_f8f6f4 v[62:65], v[26:33], v[210:217], 0, v191, v192 op_sel_hi:[0,0,0]
	v_mfma_scale_f32_16x16x128_f8f6f4 v[58:61], v[18:25], v[210:217], 0, v191, v192 op_sel_hi:[0,0,0]
	v_mfma_scale_f32_16x16x128_f8f6f4 v[46:49], v[26:33], v[218:225], 0, v191, v192 op_sel_hi:[0,0,0]
	v_mfma_scale_f32_16x16x128_f8f6f4 v[42:45], v[18:25], v[218:225], 0, v191, v192 op_sel_hi:[0,0,0]
	s_setprio 0
	s_setprio 1
	s_nop 3
	v_mfma_scale_f32_16x16x128_f8f6f4 v[86:89], v[10:17], v[194:201], 0, v191, v192 op_sel_hi:[0,0,0]
	v_mfma_scale_f32_16x16x128_f8f6f4 v[82:85], v[2:9], v[194:201], 0, v191, v192 op_sel_hi:[0,0,0]
	v_mfma_scale_f32_16x16x128_f8f6f4 v[70:73], v[10:17], v[202:209], 0, v191, v192 op_sel_hi:[0,0,0]
	v_mfma_scale_f32_16x16x128_f8f6f4 v[66:69], v[2:9], v[202:209], 0, v191, v192 op_sel_hi:[0,0,0]
	v_mfma_scale_f32_16x16x128_f8f6f4 v[54:57], v[10:17], v[210:217], 0, v191, v192 op_sel_hi:[0,0,0]
	v_mfma_scale_f32_16x16x128_f8f6f4 v[50:53], v[2:9], v[210:217], 0, v191, v192 op_sel_hi:[0,0,0]
	v_mfma_scale_f32_16x16x128_f8f6f4 v[38:41], v[10:17], v[218:225], 0, v191, v192 op_sel_hi:[0,0,0]
	v_mfma_scale_f32_16x16x128_f8f6f4 v[34:37], v[2:9], v[218:225], 0, v191, v192 op_sel_hi:[0,0,0]
	s_setprio 0
	s_barrier
; #define PG8_STAGE(bufoff, gbase, voff) do { _Pragma("unroll") for (int _i = 0; _i < 2; ++_i) \
;         __builtin_amdgcn_global_load_lds((const unsigned*)((const char*)(gbase) + (voff)[_i]), (PG8_LAS unsigned*)(lds + (bufoff) + ldsw + _i * 8192), 16, 0, 0); } while (0)
; #define PG8_STAGE_A(bufoff, gbase, h, nx) do { if constexpr (Sched::GATHER) { const unsigned vv_[2] = {(nx) ? vAn[h][0] : vA[h][0], (nx) ? vAn[h][1] : vA[h][1]}; PG8_STAGE(bufoff, gbase, vv_); } \
;         else { PG8_STAGE(bufoff, (gbase) + (h) * hstep, voffA); } } while (0)
; #define PG8_LDA(dst, b, h) do { _Pragma("unroll") for (int m = 0; m < 4; ++m) _Pragma("unroll") for (int k = 0; k < 2; ++k) dst[m][k] = *(const PG8_LAS bf16x8*)(lds + PG8_SA(b, h) + aoff + m * 2048 + k * 1024); } while (0)
; #define PG8_LDB(dst, b, h) do { _Pragma("unroll") for (int n = 0; n < 2; ++n) _Pragma("unroll") for (int k = 0; k < 2; ++k) dst[n][k] = *(const PG8_LAS bf16x8*)(lds + PG8_SB(b, h) + boff + n * 2048 + k * 1024); } while (0)
; #define PG8_WAIT_V(n) asm volatile("s_waitcnt vmcnt(" #n ")" ::: "memory")
; #define PG8_WAIT_L(n) asm volatile("s_waitcnt lgkmcnt(" #n ")" ::: "memory")
; #define PG8_BAR __builtin_amdgcn_s_barrier()
; #define PG8_SCHED __builtin_amdgcn_sched_barrier(0)
;     ...
;             PG8_LDB(B0, 1, 0); PG8_LDB(B1, 1, 1); PG8_SCHED; PG8_LDA(At, 1, 0); PG8_STAGE_A(PG8_SA(0, 1), a2, 1, last);
;             PG8_WAIT_V(8); PG8_WAIT_L(0); PG8_BAR; PG8_MMA(0, 0, At, B0); PG8_MMA(0, 1, At, B1); PG8_BAR; PG8_SCHED;
;             PG8_LDA(At, 1, 1); PG8_STAGE(PG8_SB(1, 0), b3, voffB); PG8_STAGE(PG8_SB(1, 1), b3 + hstepB, voffB); PG8_STAGE_A(PG8_SA(1, 0), a3, 0, last);
;             PG8_WAIT_V(8); PG8_WAIT_L(0); PG8_BAR; PG8_MMA(1, 0, At, B0); PG8_MMA(1, 1, At, B1); PG8_BAR; PG8_SCHED;
	s_add_i32 s51, 0, 0x18000
	s_add_i32 s52, 0, 0x1c000
	v_add_u32_e32 v14, s51, v186
	v_add_u32_e32 v30, s52, v186
	ds_read_b128 v[2:5], v14
	ds_read_b128 v[6:9], v14 offset:1024
	ds_read_b128 v[10:13], v14 offset:2048
	ds_read_b128 v[14:17], v14 offset:3072
	ds_read_b128 v[18:21], v30
	ds_read_b128 v[22:25], v30 offset:1024
	ds_read_b128 v[26:29], v30 offset:2048
	ds_read_b128 v[30:33], v30 offset:3072
	s_add_u32 s26, s26, 0x40000
	s_addc_u32 s27, s27, 0
	s_mov_b32 m0, s30
	v_lshl_add_u64 v[226:227], s[26:27], 0, v[168:169]
	ds_read_b128 v[194:197], v190 offset:32768
	ds_read_b128 v[198:201], v190 offset:33792
	ds_read_b128 v[202:205], v190 offset:34816
	ds_read_b128 v[206:209], v190 offset:35840
	ds_read_b128 v[210:213], v190 offset:36864
	ds_read_b128 v[214:217], v190 offset:37888
	ds_read_b128 v[218:221], v190 offset:38912
	ds_read_b128 v[222:225], v190 offset:39936
	global_load_lds_dwordx4 v[226:227], off
	v_lshl_add_u64 v[226:227], s[26:27], 0, v[164:165]
	s_mov_b32 m0, s31
	s_nop 0
	global_load_lds_dwordx4 v[226:227], off
	s_waitcnt vmcnt(8)
	s_waitcnt lgkmcnt(0)
	s_barrier
	s_setprio 1
	s_nop 3
	s_waitcnt lgkmcnt(0)
	v_mfma_scale_f32_16x16x128_f8f6f4 v[158:161], v[2:9], v[194:201], v[158:161], v191, v192 op_sel_hi:[0,0,0]
	v_mfma_scale_f32_16x16x128_f8f6f4 v[154:157], v[10:17], v[194:201], v[154:157], v191, v192 op_sel_hi:[0,0,0]
	v_mfma_scale_f32_16x16x128_f8f6f4 v[142:145], v[2:9], v[202:209], v[142:145], v191, v192 op_sel_hi:[0,0,0]
	v_mfma_scale_f32_16x16x128_f8f6f4 v[138:141], v[10:17], v[202:209], v[138:141], v191, v192 op_sel_hi:[0,0,0]
	v_mfma_scale_f32_16x16x128_f8f6f4 v[126:129], v[2:9], v[210:217], v[126:129], v191, v192 op_sel_hi:[0,0,0]
	v_mfma_scale_f32_16x16x128_f8f6f4 v[122:125], v[10:17], v[210:217], v[122:125], v191, v192 op_sel_hi:[0,0,0]
	v_mfma_scale_f32_16x16x128_f8f6f4 v[110:113], v[2:9], v[218:225], v[110:113], v191, v192 op_sel_hi:[0,0,0]
	v_mfma_scale_f32_16x16x128_f8f6f4 v[106:109], v[10:17], v[218:225], v[106:109], v191, v192 op_sel_hi:[0,0,0]
	s_setprio 0
	s_setprio 1
	s_nop 3
	v_mfma_scale_f32_16x16x128_f8f6f4 v[150:153], v[18:25], v[194:201], v[150:153], v191, v192 op_sel_hi:[0,0,0]
	v_mfma_scale_f32_16x16x128_f8f6f4 v[146:149], v[26:33], v[194:201], v[146:149], v191, v192 op_sel_hi:[0,0,0]
	v_mfma_scale_f32_16x16x128_f8f6f4 v[134:137], v[18:25], v[202:209], v[134:137], v191, v192 op_sel_hi:[0,0,0]
	v_mfma_scale_f32_16x16x128_f8f6f4 v[130:133], v[26:33], v[202:209], v[130:133], v191, v192 op_sel_hi:[0,0,0]
	v_mfma_scale_f32_16x16x128_f8f6f4 v[118:121], v[18:25], v[210:217], v[118:121], v191, v192 op_sel_hi:[0,0,0]
	v_mfma_scale_f32_16x16x128_f8f6f4 v[114:117], v[26:33], v[210:217], v[114:117], v191, v192 op_sel_hi:[0,0,0]
	v_mfma_scale_f32_16x16x128_f8f6f4 v[102:105], v[18:25], v[218:225], v[102:105], v191, v192 op_sel_hi:[0,0,0]
	v_mfma_scale_f32_16x16x128_f8f6f4 v[98:101], v[26:33], v[218:225], v[98:101], v191, v192 op_sel_hi:[0,0,0]
	s_setprio 0
	s_barrier
	s_add_i32 s26, s51, s21
	v_lshl_add_u64 v[178:179], v[178:179], 0, s[8:9]
	s_mov_b32 m0, s26
	ds_read_b128 v[194:197], v190 offset:49152
	ds_read_b128 v[198:201], v190 offset:50176
	ds_read_b128 v[202:205], v190 offset:51200
	ds_read_b128 v[206:209], v190 offset:52224
	ds_read_b128 v[210:213], v190 offset:53248
	ds_read_b128 v[214:217], v190 offset:54272
	ds_read_b128 v[218:221], v190 offset:55296
	ds_read_b128 v[222:225], v190 offset:56320
	global_load_lds_dwordx4 v[178:179], off
	s_add_i32 m0, s26, 0x2000
	s_add_u32 s24, s24, 0x4080
	v_lshl_add_u64 v[178:179], v[180:181], 0, s[8:9]
	s_addc_u32 s25, s25, 0
	s_add_i32 s26, s52, s21
	global_load_lds_dwordx4 v[178:179], off
	v_lshl_add_u64 v[178:179], s[24:25], 0, v[166:167]
	s_mov_b32 m0, s26
	s_nop 0
	global_load_lds_dwordx4 v[178:179], off
	v_lshl_add_u64 v[178:179], s[24:25], 0, v[162:163]
	s_add_i32 m0, s26, 0x2000
	s_nop 0
	global_load_lds_dwordx4 v[178:179], off
	v_lshl_add_u64 v[178:179], v[182:183], 0, s[8:9]
	s_mov_b32 m0, s36
	s_nop 0
	global_load_lds_dwordx4 v[178:179], off
	v_lshl_add_u64 v[178:179], v[184:185], 0, s[8:9]
	s_mov_b32 m0, s37
	s_nop 0
	global_load_lds_dwordx4 v[178:179], off
	s_waitcnt vmcnt(8)
	s_waitcnt lgkmcnt(0)
	s_barrier
	s_setprio 1
	s_nop 3
	s_waitcnt lgkmcnt(0)
	v_mfma_scale_f32_16x16x128_f8f6f4 v[94:97], v[2:9], v[194:201], v[94:97], v191, v192 op_sel_hi:[0,0,0]
	v_mfma_scale_f32_16x16x128_f8f6f4 v[90:93], v[10:17], v[194:201], v[90:93], v191, v192 op_sel_hi:[0,0,0]
	v_mfma_scale_f32_16x16x128_f8f6f4 v[78:81], v[2:9], v[202:209], v[78:81], v191, v192 op_sel_hi:[0,0,0]
	v_mfma_scale_f32_16x16x128_f8f6f4 v[74:77], v[10:17], v[202:209], v[74:77], v191, v192 op_sel_hi:[0,0,0]
	v_mfma_scale_f32_16x16x128_f8f6f4 v[62:65], v[2:9], v[210:217], v[62:65], v191, v192 op_sel_hi:[0,0,0]
	v_mfma_scale_f32_16x16x128_f8f6f4 v[58:61], v[10:17], v[210:217], v[58:61], v191, v192 op_sel_hi:[0,0,0]
	v_mfma_scale_f32_16x16x128_f8f6f4 v[46:49], v[2:9], v[218:225], v[46:49], v191, v192 op_sel_hi:[0,0,0]
	v_mfma_scale_f32_16x16x128_f8f6f4 v[42:45], v[10:17], v[218:225], v[42:45], v191, v192 op_sel_hi:[0,0,0]
	s_setprio 0
	s_setprio 1
	s_nop 3
	v_mfma_scale_f32_16x16x128_f8f6f4 v[86:89], v[18:25], v[194:201], v[86:89], v191, v192 op_sel_hi:[0,0,0]
	v_mfma_scale_f32_16x16x128_f8f6f4 v[82:85], v[26:33], v[194:201], v[82:85], v191, v192 op_sel_hi:[0,0,0]
	v_mfma_scale_f32_16x16x128_f8f6f4 v[70:73], v[18:25], v[202:209], v[70:73], v191, v192 op_sel_hi:[0,0,0]
	v_mfma_scale_f32_16x16x128_f8f6f4 v[66:69], v[26:33], v[202:209], v[66:69], v191, v192 op_sel_hi:[0,0,0]
	v_mfma_scale_f32_16x16x128_f8f6f4 v[54:57], v[18:25], v[210:217], v[54:57], v191, v192 op_sel_hi:[0,0,0]
	v_mfma_scale_f32_16x16x128_f8f6f4 v[50:53], v[26:33], v[210:217], v[50:53], v191, v192 op_sel_hi:[0,0,0]
	v_mfma_scale_f32_16x16x128_f8f6f4 v[38:41], v[18:25], v[218:225], v[38:41], v191, v192 op_sel_hi:[0,0,0]
	v_mfma_scale_f32_16x16x128_f8f6f4 v[34:37], v[26:33], v[218:225], v[34:37], v191, v192 op_sel_hi:[0,0,0]
	s_setprio 0
	s_barrier
	s_add_i32 s50, s50, 2
	s_add_u32 s22, s22, 0x100
	s_addc_u32 s23, s23, 0
	s_add_u32 s48, s48, 0x100
	s_addc_u32 s49, s49, 0
; #define PG8_STAGE(bufoff, gbase, voff) do { _Pragma("unroll") for (int _i = 0; _i < 2; ++_i) \
;         __builtin_amdgcn_global_load_lds((const unsigned*)((const char*)(gbase) + (voff)[_i]), (PG8_LAS unsigned*)(lds + (bufoff) + ldsw + _i * 8192), 16, 0, 0); } while (0)
; #define PG8_STAGE_A(bufoff, gbase, h, nx) do { if constexpr (Sched::GATHER) { const unsigned vv_[2] = {(nx) ? vAn[h][0] : vA[h][0], (nx) ? vAn[h][1] : vA[h][1]}; PG8_STAGE(bufoff, gbase, vv_); } \
;         else { PG8_STAGE(bufoff, (gbase) + (h) * hstep, voffA); } } while (0)
; #define PG8_LDA(dst, b, h) do { _Pragma("unroll") for (int m = 0; m < 4; ++m) _Pragma("unroll") for (int k = 0; k < 2; ++k) dst[m][k] = *(const PG8_LAS bf16x8*)(lds + PG8_SA(b, h) + aoff + m * 2048 + k * 1024); } while (0)
; #define PG8_LDB(dst, b, h) do { _Pragma("unroll") for (int n = 0; n < 2; ++n) _Pragma("unroll") for (int k = 0; k < 2; ++k) dst[n][k] = *(const PG8_LAS bf16x8*)(lds + PG8_SB(b, h) + boff + n * 2048 + k * 1024); } while (0)
; #define PG8_WAIT_V(n) asm volatile("s_waitcnt vmcnt(" #n ")" ::: "memory")
; #define PG8_WAIT_L(n) asm volatile("s_waitcnt lgkmcnt(" #n ")" ::: "memory")
; #define PG8_BAR __builtin_amdgcn_s_barrier()
; #define PG8_SCHED __builtin_amdgcn_sched_barrier(0)
;     ...
;         for (int t = 0; t < nt; t += 2) {
;             const bool last = (t == nt - 2);
;             const char* a1 = cA + (size_t)(t + 1) * kstep;
;             const char* a2 = last ? nA : cA + (size_t)(t + 2) * kstep; const char* b2 = last ? nB : cB + (size_t)(t + 2) * kstep;
;             const char* a3 = a2 + kstep; const char* b3 = b2 + kstep;
;             if (last && has_next) S.a_ready(nxt);
;             if constexpr (SP2) {
;             PG8_LDB(B0, 0, 0); PG8_LDB(B1, 0, 1); PG8_SCHED; PG8_LDA(At, 0, 0); PG8_STAGE_A(PG8_SA(1, 1), a1, 1, false);
;             PG8_WAIT_V(8); PG8_WAIT_L(0); PG8_BAR; PG8_MMA(0, 0, At, B0); PG8_MMA(0, 1, At, B1); PG8_BAR; PG8_SCHED;
;             PG8_LDA(At, 0, 1); PG8_STAGE(PG8_SB(0, 0), b2, voffB); PG8_STAGE(PG8_SB(0, 1), b2 + hstepB, voffB); PG8_STAGE_A(PG8_SA(0, 0), a2, 0, last);
;             PG8_WAIT_V(8); PG8_WAIT_L(0); PG8_BAR; PG8_MMA(1, 0, At, B0); PG8_MMA(1, 1, At, B1); PG8_BAR; PG8_SCHED;
.LBB0_1626:
	ds_read_b128 v[26:29], v188
	ds_read_b128 v[30:33], v188 offset:1024
	ds_read_b128 v[18:21], v188 offset:2048
	ds_read_b128 v[22:25], v188 offset:3072
	ds_read_b128 v[10:13], v189
	ds_read_b128 v[14:17], v189 offset:1024
	ds_read_b128 v[2:5], v189 offset:2048
	ds_read_b128 v[6:9], v189 offset:3072
	s_add_u32 s24, s22, 0xfffc0080
	s_addc_u32 s25, s23, -1
	s_cmp_eq_u32 s50, 12
	s_cselect_b32 s27, s13, s25
	s_cselect_b32 s26, s46, s24
	s_cselect_b32 s25, s15, s49
	s_cselect_b32 s24, s47, s48
	v_lshl_add_u64 v[218:219], s[22:23], 0, v[170:171]
	s_add_i32 m0, s28, 0xc000
	ds_read_b128 v[178:181], v190
	ds_read_b128 v[182:185], v190 offset:1024
	ds_read_b128 v[194:197], v190 offset:2048
	ds_read_b128 v[198:201], v190 offset:3072
	ds_read_b128 v[202:205], v190 offset:4096
	ds_read_b128 v[206:209], v190 offset:5120
	ds_read_b128 v[210:213], v190 offset:6144
	ds_read_b128 v[214:217], v190 offset:7168
	global_load_lds_dwordx4 v[218:219], off
	v_lshl_add_u64 v[218:219], s[22:23], 0, v[172:173]
	s_add_i32 m0, s28, 0xe000
	s_nop 0
	global_load_lds_dwordx4 v[218:219], off
	s_waitcnt vmcnt(8)
	s_waitcnt lgkmcnt(0)
	s_barrier
	s_setprio 1
	s_nop 3
	s_waitcnt lgkmcnt(0)
	v_mfma_scale_f32_16x16x128_f8f6f4 v[158:161], v[26:33], v[178:185], v[158:161], v191, v192 op_sel_hi:[0,0,0]
	v_mfma_scale_f32_16x16x128_f8f6f4 v[154:157], v[18:25], v[178:185], v[154:157], v191, v192 op_sel_hi:[0,0,0]
	v_mfma_scale_f32_16x16x128_f8f6f4 v[142:145], v[26:33], v[194:201], v[142:145], v191, v192 op_sel_hi:[0,0,0]
	v_mfma_scale_f32_16x16x128_f8f6f4 v[138:141], v[18:25], v[194:201], v[138:141], v191, v192 op_sel_hi:[0,0,0]
	v_mfma_scale_f32_16x16x128_f8f6f4 v[126:129], v[26:33], v[202:209], v[126:129], v191, v192 op_sel_hi:[0,0,0]
	v_mfma_scale_f32_16x16x128_f8f6f4 v[122:125], v[18:25], v[202:209], v[122:125], v191, v192 op_sel_hi:[0,0,0]
	v_mfma_scale_f32_16x16x128_f8f6f4 v[110:113], v[26:33], v[210:217], v[110:113], v191, v192 op_sel_hi:[0,0,0]
	v_mfma_scale_f32_16x16x128_f8f6f4 v[106:109], v[18:25], v[210:217], v[106:109], v191, v192 op_sel_hi:[0,0,0]
	s_setprio 0
	s_setprio 1
	s_nop 3
	v_mfma_scale_f32_16x16x128_f8f6f4 v[150:153], v[10:17], v[178:185], v[150:153], v191, v192 op_sel_hi:[0,0,0]
	v_mfma_scale_f32_16x16x128_f8f6f4 v[146:149], v[2:9], v[178:185], v[146:149], v191, v192 op_sel_hi:[0,0,0]
	v_mfma_scale_f32_16x16x128_f8f6f4 v[134:137], v[10:17], v[194:201], v[134:137], v191, v192 op_sel_hi:[0,0,0]
	v_mfma_scale_f32_16x16x128_f8f6f4 v[130:133], v[2:9], v[194:201], v[130:133], v191, v192 op_sel_hi:[0,0,0]
	v_mfma_scale_f32_16x16x128_f8f6f4 v[118:121], v[10:17], v[202:209], v[118:121], v191, v192 op_sel_hi:[0,0,0]
	v_mfma_scale_f32_16x16x128_f8f6f4 v[114:117], v[2:9], v[202:209], v[114:117], v191, v192 op_sel_hi:[0,0,0]
	v_mfma_scale_f32_16x16x128_f8f6f4 v[102:105], v[10:17], v[210:217], v[102:105], v191, v192 op_sel_hi:[0,0,0]
	v_mfma_scale_f32_16x16x128_f8f6f4 v[98:101], v[2:9], v[210:217], v[98:101], v191, v192 op_sel_hi:[0,0,0]
	s_setprio 0
	s_barrier
	s_add_i32 s51, s39, s21
	v_lshl_add_u64 v[178:179], s[24:25], 0, v[166:167]
	s_mov_b32 m0, s51
	ds_read_b128 v[194:197], v190 offset:16384
	ds_read_b128 v[198:201], v190 offset:17408
	ds_read_b128 v[202:205], v190 offset:18432
	ds_read_b128 v[206:209], v190 offset:19456
	ds_read_b128 v[210:213], v190 offset:20480
	ds_read_b128 v[214:217], v190 offset:21504
	ds_read_b128 v[218:221], v190 offset:22528
	ds_read_b128 v[222:225], v190 offset:23552
	global_load_lds_dwordx4 v[178:179], off
	s_add_i32 m0, s51, 0x2000
	s_add_u32 s52, s24, 0x4000
	v_lshl_add_u64 v[180:181], s[24:25], 0, v[162:163]
	s_addc_u32 s53, s25, 0
	s_add_i32 s51, s40, s21
	global_load_lds_dwordx4 v[180:181], off
	v_lshl_add_u64 v[182:183], s[52:53], 0, v[166:167]
	s_mov_b32 m0, s51
	v_lshl_add_u64 v[184:185], s[26:27], 0, v[164:165]
	global_load_lds_dwordx4 v[182:183], off
	v_lshl_add_u64 v[182:183], s[52:53], 0, v[162:163]
	s_add_i32 m0, s51, 0x2000
	s_nop 0
	global_load_lds_dwordx4 v[182:183], off
	v_lshl_add_u64 v[182:183], s[26:27], 0, v[168:169]
	s_mov_b32 m0, s28
	s_nop 0
	global_load_lds_dwordx4 v[182:183], off
	s_mov_b32 m0, s29
	s_nop 0
	global_load_lds_dwordx4 v[184:185], off
	s_waitcnt vmcnt(8)
	s_waitcnt lgkmcnt(0)
	s_barrier
	s_setprio 1
	s_nop 3
	s_waitcnt lgkmcnt(0)
	v_mfma_scale_f32_16x16x128_f8f6f4 v[94:97], v[26:33], v[194:201], v[94:97], v191, v192 op_sel_hi:[0,0,0]
	v_mfma_scale_f32_16x16x128_f8f6f4 v[90:93], v[18:25], v[194:201], v[90:93], v191, v192 op_sel_hi:[0,0,0]
	v_mfma_scale_f32_16x16x128_f8f6f4 v[78:81], v[26:33], v[202:209], v[78:81], v191, v192 op_sel_hi:[0,0,0]
	v_mfma_scale_f32_16x16x128_f8f6f4 v[74:77], v[18:25], v[202:209], v[74:77], v191, v192 op_sel_hi:[0,0,0]
	v_mfma_scale_f32_16x16x128_f8f6f4 v[62:65], v[26:33], v[210:217], v[62:65], v191, v192 op_sel_hi:[0,0,0]
	v_mfma_scale_f32_16x16x128_f8f6f4 v[58:61], v[18:25], v[210:217], v[58:61], v191, v192 op_sel_hi:[0,0,0]
	v_mfma_scale_f32_16x16x128_f8f6f4 v[46:49], v[26:33], v[218:225], v[46:49], v191, v192 op_sel_hi:[0,0,0]
	v_mfma_scale_f32_16x16x128_f8f6f4 v[42:45], v[18:25], v[218:225], v[42:45], v191, v192 op_sel_hi:[0,0,0]
	s_setprio 0
	s_setprio 1
	s_nop 3
	v_mfma_scale_f32_16x16x128_f8f6f4 v[86:89], v[10:17], v[194:201], v[86:89], v191, v192 op_sel_hi:[0,0,0]
	v_mfma_scale_f32_16x16x128_f8f6f4 v[82:85], v[2:9], v[194:201], v[82:85], v191, v192 op_sel_hi:[0,0,0]
	v_mfma_scale_f32_16x16x128_f8f6f4 v[70:73], v[10:17], v[202:209], v[70:73], v191, v192 op_sel_hi:[0,0,0]
	v_mfma_scale_f32_16x16x128_f8f6f4 v[66:69], v[2:9], v[202:209], v[66:69], v191, v192 op_sel_hi:[0,0,0]
	v_mfma_scale_f32_16x16x128_f8f6f4 v[54:57], v[10:17], v[210:217], v[54:57], v191, v192 op_sel_hi:[0,0,0]
	v_mfma_scale_f32_16x16x128_f8f6f4 v[50:53], v[2:9], v[210:217], v[50:53], v191, v192 op_sel_hi:[0,0,0]
	v_mfma_scale_f32_16x16x128_f8f6f4 v[38:41], v[10:17], v[218:225], v[38:41], v191, v192 op_sel_hi:[0,0,0]
	v_mfma_scale_f32_16x16x128_f8f6f4 v[34:37], v[2:9], v[218:225], v[34:37], v191, v192 op_sel_hi:[0,0,0]
	s_setprio 0
	s_barrier
; #define PG8_STAGE(bufoff, gbase, voff) do { _Pragma("unroll") for (int _i = 0; _i < 2; ++_i) \
;         __builtin_amdgcn_global_load_lds((const unsigned*)((const char*)(gbase) + (voff)[_i]), (PG8_LAS unsigned*)(lds + (bufoff) + ldsw + _i * 8192), 16, 0, 0); } while (0)
; #define PG8_WAIT_V(n) asm volatile("s_waitcnt vmcnt(" #n ")" ::: "memory")
; #define PG8_WAIT_L(n) asm volatile("s_waitcnt lgkmcnt(" #n ")" ::: "memory")
;     ...
;             PG8_LDB(B0, 1, 0); PG8_LDB(B1, 1, 1); PG8_SCHED; PG8_LDA(At, 1, 0); PG8_STAGE_A(PG8_SA(0, 1), a2, 1, last);
;             PG8_WAIT_V(8); PG8_WAIT_L(0); PG8_BAR; PG8_MMA(0, 0, At, B0); PG8_MMA(0, 1, At, B1); PG8_BAR; PG8_SCHED;
;             PG8_LDA(At, 1, 1); PG8_STAGE(PG8_SB(1, 0), b3, voffB); PG8_STAGE(PG8_SB(1, 1), b3 + hstepB, voffB); PG8_STAGE_A(PG8_SA(1, 0), a3, 0, last);
;             PG8_WAIT_V(8); PG8_WAIT_L(0); PG8_BAR; PG8_MMA(1, 0, At, B0); PG8_MMA(1, 1, At, B1); PG8_BAR; PG8_SCHED;
;             } else {
;             PG8_LDB(B0, 0, 0); PG8_SCHED; PG8_LDA(At, 0, 0); PG8_STAGE(PG8_SA(1, 1), a1 + hstep, voffA);
;             PG8_WAIT_L(8); PG8_BAR; PG8_WAIT_L(0); PG8_MMA(0, 0, At, B0); PG8_BAR; PG8_SCHED;
;             PG8_LDB(B1, 0, 1); PG8_STAGE(PG8_SB(0, 0), b2, voffB);
;             PG8_BAR; PG8_WAIT_L(0); PG8_MMA(0, 1, At, B1); PG8_BAR;
;             PG8_LDA(At, 0, 1); PG8_STAGE(PG8_SA(0, 0), a2, voffA);
;             PG8_BAR; PG8_WAIT_L(0); PG8_MMA(1, 0, At, B0); PG8_BAR; PG8_SCHED;
;             PG8_STAGE(PG8_SB(0, 1), b2 + hstepB, voffB);
;             PG8_WAIT_V(6); PG8_BAR; PG8_MMA(1, 1, At, B1); PG8_BAR;
;             PG8_LDB(B0, 1, 0); PG8_SCHED; PG8_LDA(At, 1, 0); PG8_STAGE(PG8_SA(0, 1), a2 + hstep, voffA);
;             PG8_WAIT_L(8); PG8_BAR; PG8_WAIT_L(0); PG8_MMA(0, 0, At, B0); PG8_BAR; PG8_SCHED;
;             PG8_LDB(B1, 1, 1); PG8_STAGE(PG8_SB(1, 0), b3, voffB);
;             PG8_BAR; PG8_WAIT_L(0); PG8_MMA(0, 1, At, B1); PG8_BAR;
;             PG8_LDA(At, 1, 1); PG8_STAGE(PG8_SA(1, 0), a3, voffA);
;             PG8_BAR; PG8_WAIT_L(0); PG8_MMA(1, 0, At, B0); PG8_BAR; PG8_SCHED;
;             PG8_STAGE(PG8_SB(1, 1), b3 + hstepB, voffB);
;             PG8_WAIT_V(6); PG8_BAR; PG8_MMA(1, 1, At, B1); PG8_BAR;
;             }
;         }
;         if constexpr (F8) asm volatile("s_nop 15\n\ts_nop 15\n\ts_nop 15" ::: "memory");
;         if constexpr (ALIGN_EPI) { if (wr == 0) PG8_BAR; }
	s_add_i32 s51, 0, 0x18000
	s_add_i32 s52, 0, 0x1c000
	v_add_u32_e32 v14, s51, v186
	v_add_u32_e32 v30, s52, v186
	ds_read_b128 v[2:5], v14
	ds_read_b128 v[6:9], v14 offset:1024
	ds_read_b128 v[10:13], v14 offset:2048
	ds_read_b128 v[14:17], v14 offset:3072
	ds_read_b128 v[18:21], v30
	ds_read_b128 v[22:25], v30 offset:1024
	ds_read_b128 v[26:29], v30 offset:2048
	ds_read_b128 v[30:33], v30 offset:3072
	s_add_u32 s26, s26, 0x40000
	s_addc_u32 s27, s27, 0
	s_mov_b32 m0, s30
	v_lshl_add_u64 v[226:227], s[26:27], 0, v[168:169]
	ds_read_b128 v[194:197], v190 offset:32768
	ds_read_b128 v[198:201], v190 offset:33792
	ds_read_b128 v[202:205], v190 offset:34816
	ds_read_b128 v[206:209], v190 offset:35840
	ds_read_b128 v[210:213], v190 offset:36864
	ds_read_b128 v[214:217], v190 offset:37888
	ds_read_b128 v[218:221], v190 offset:38912
	ds_read_b128 v[222:225], v190 offset:39936
	global_load_lds_dwordx4 v[226:227], off
	v_lshl_add_u64 v[226:227], s[26:27], 0, v[164:165]
	s_mov_b32 m0, s31
	s_nop 0
	global_load_lds_dwordx4 v[226:227], off
	s_waitcnt vmcnt(8)
	s_waitcnt lgkmcnt(0)
	s_barrier
	s_setprio 1
	s_nop 3
	s_waitcnt lgkmcnt(0)
	v_mfma_scale_f32_16x16x128_f8f6f4 v[158:161], v[2:9], v[194:201], v[158:161], v191, v192 op_sel_hi:[0,0,0]
	v_mfma_scale_f32_16x16x128_f8f6f4 v[154:157], v[10:17], v[194:201], v[154:157], v191, v192 op_sel_hi:[0,0,0]
	v_mfma_scale_f32_16x16x128_f8f6f4 v[142:145], v[2:9], v[202:209], v[142:145], v191, v192 op_sel_hi:[0,0,0]
	v_mfma_scale_f32_16x16x128_f8f6f4 v[138:141], v[10:17], v[202:209], v[138:141], v191, v192 op_sel_hi:[0,0,0]
	v_mfma_scale_f32_16x16x128_f8f6f4 v[126:129], v[2:9], v[210:217], v[126:129], v191, v192 op_sel_hi:[0,0,0]
	v_mfma_scale_f32_16x16x128_f8f6f4 v[122:125], v[10:17], v[210:217], v[122:125], v191, v192 op_sel_hi:[0,0,0]
	v_mfma_scale_f32_16x16x128_f8f6f4 v[110:113], v[2:9], v[218:225], v[110:113], v191, v192 op_sel_hi:[0,0,0]
	v_mfma_scale_f32_16x16x128_f8f6f4 v[106:109], v[10:17], v[218:225], v[106:109], v191, v192 op_sel_hi:[0,0,0]
	s_setprio 0
	s_setprio 1
	s_nop 3
	v_mfma_scale_f32_16x16x128_f8f6f4 v[150:153], v[18:25], v[194:201], v[150:153], v191, v192 op_sel_hi:[0,0,0]
	v_mfma_scale_f32_16x16x128_f8f6f4 v[146:149], v[26:33], v[194:201], v[146:149], v191, v192 op_sel_hi:[0,0,0]
	v_mfma_scale_f32_16x16x128_f8f6f4 v[134:137], v[18:25], v[202:209], v[134:137], v191, v192 op_sel_hi:[0,0,0]
	v_mfma_scale_f32_16x16x128_f8f6f4 v[130:133], v[26:33], v[202:209], v[130:133], v191, v192 op_sel_hi:[0,0,0]
	v_mfma_scale_f32_16x16x128_f8f6f4 v[118:121], v[18:25], v[210:217], v[118:121], v191, v192 op_sel_hi:[0,0,0]
	v_mfma_scale_f32_16x16x128_f8f6f4 v[114:117], v[26:33], v[210:217], v[114:117], v191, v192 op_sel_hi:[0,0,0]
	v_mfma_scale_f32_16x16x128_f8f6f4 v[102:105], v[18:25], v[218:225], v[102:105], v191, v192 op_sel_hi:[0,0,0]
	v_mfma_scale_f32_16x16x128_f8f6f4 v[98:101], v[26:33], v[218:225], v[98:101], v191, v192 op_sel_hi:[0,0,0]
	s_setprio 0
	s_barrier
	s_add_i32 s26, s51, s21
	v_lshl_add_u64 v[178:179], v[178:179], 0, s[8:9]
	s_mov_b32 m0, s26
	ds_read_b128 v[194:197], v190 offset:49152
	ds_read_b128 v[198:201], v190 offset:50176
	ds_read_b128 v[202:205], v190 offset:51200
	ds_read_b128 v[206:209], v190 offset:52224
	ds_read_b128 v[210:213], v190 offset:53248
	ds_read_b128 v[214:217], v190 offset:54272
	ds_read_b128 v[218:221], v190 offset:55296
	ds_read_b128 v[222:225], v190 offset:56320
	global_load_lds_dwordx4 v[178:179], off
	s_add_i32 m0, s26, 0x2000
	s_add_u32 s24, s24, 0x4080
	v_lshl_add_u64 v[178:179], v[180:181], 0, s[8:9]
	s_addc_u32 s25, s25, 0
	s_add_i32 s26, s52, s21
	global_load_lds_dwordx4 v[178:179], off
	v_lshl_add_u64 v[178:179], s[24:25], 0, v[166:167]
	s_mov_b32 m0, s26
	s_nop 0
	global_load_lds_dwordx4 v[178:179], off
	v_lshl_add_u64 v[178:179], s[24:25], 0, v[162:163]
	s_add_i32 m0, s26, 0x2000
	s_nop 0
	global_load_lds_dwordx4 v[178:179], off
	v_lshl_add_u64 v[178:179], v[182:183], 0, s[8:9]
	s_mov_b32 m0, s36
	s_nop 0
	global_load_lds_dwordx4 v[178:179], off
	v_lshl_add_u64 v[178:179], v[184:185], 0, s[8:9]
	s_mov_b32 m0, s37
	s_nop 0
	global_load_lds_dwordx4 v[178:179], off
	s_waitcnt vmcnt(8)
	s_waitcnt lgkmcnt(0)
	s_barrier
	s_setprio 1
	s_nop 3
	s_waitcnt lgkmcnt(0)
	v_mfma_scale_f32_16x16x128_f8f6f4 v[94:97], v[2:9], v[194:201], v[94:97], v191, v192 op_sel_hi:[0,0,0]
	v_mfma_scale_f32_16x16x128_f8f6f4 v[90:93], v[10:17], v[194:201], v[90:93], v191, v192 op_sel_hi:[0,0,0]
	v_mfma_scale_f32_16x16x128_f8f6f4 v[78:81], v[2:9], v[202:209], v[78:81], v191, v192 op_sel_hi:[0,0,0]
	v_mfma_scale_f32_16x16x128_f8f6f4 v[74:77], v[10:17], v[202:209], v[74:77], v191, v192 op_sel_hi:[0,0,0]
	v_mfma_scale_f32_16x16x128_f8f6f4 v[62:65], v[2:9], v[210:217], v[62:65], v191, v192 op_sel_hi:[0,0,0]
	v_mfma_scale_f32_16x16x128_f8f6f4 v[58:61], v[10:17], v[210:217], v[58:61], v191, v192 op_sel_hi:[0,0,0]
	v_mfma_scale_f32_16x16x128_f8f6f4 v[46:49], v[2:9], v[218:225], v[46:49], v191, v192 op_sel_hi:[0,0,0]
	v_mfma_scale_f32_16x16x128_f8f6f4 v[42:45], v[10:17], v[218:225], v[42:45], v191, v192 op_sel_hi:[0,0,0]
	s_setprio 0
	s_setprio 1
	s_nop 3
	v_mfma_scale_f32_16x16x128_f8f6f4 v[86:89], v[18:25], v[194:201], v[86:89], v191, v192 op_sel_hi:[0,0,0]
	v_mfma_scale_f32_16x16x128_f8f6f4 v[82:85], v[26:33], v[194:201], v[82:85], v191, v192 op_sel_hi:[0,0,0]
	v_mfma_scale_f32_16x16x128_f8f6f4 v[70:73], v[18:25], v[202:209], v[70:73], v191, v192 op_sel_hi:[0,0,0]
	v_mfma_scale_f32_16x16x128_f8f6f4 v[66:69], v[26:33], v[202:209], v[66:69], v191, v192 op_sel_hi:[0,0,0]
	v_mfma_scale_f32_16x16x128_f8f6f4 v[54:57], v[18:25], v[210:217], v[54:57], v191, v192 op_sel_hi:[0,0,0]
	v_mfma_scale_f32_16x16x128_f8f6f4 v[50:53], v[26:33], v[210:217], v[50:53], v191, v192 op_sel_hi:[0,0,0]
	v_mfma_scale_f32_16x16x128_f8f6f4 v[38:41], v[18:25], v[218:225], v[38:41], v191, v192 op_sel_hi:[0,0,0]
	v_mfma_scale_f32_16x16x128_f8f6f4 v[34:37], v[26:33], v[218:225], v[34:37], v191, v192 op_sel_hi:[0,0,0]
	s_setprio 0
	s_barrier
	s_add_i32 s50, s50, 2
	s_add_u32 s22, s22, 0x100
	s_addc_u32 s23, s23, 0
	s_add_u32 s48, s48, 0x100
	s_addc_u32 s49, s49, 0
	s_cmp_gt_u32 s50, 13
	s_cbranch_scc0 .LBB0_1626
	s_and_b64 vcc, exec, s[10:11]
	s_cbranch_vccz .LBB0_1629
	s_barrier
; __device__ __forceinline__ unsigned pk4_fp8(float a, float b, float c, float d) { unsigned w = 0u; w = __builtin_amdgcn_cvt_pk_fp8_f32(a, b, w, false); w = __builtin_amdgcn_cvt_pk_fp8_f32(c, d, w, true); return w; }
; __device__ __forceinline__ float clamp448(float v) { return __builtin_amdgcn_fmed3f(v, -448.f, 448.f); }
;     __device__ __forceinline__ void operator()(const f32x4 (&acc)[2][2][4][2], const Unit& u, int wr, int wc, int fr, int fq) const {
;         const int row0 = u.pm * BM + wr * 64 + fr, col0 = u.pn * BM + wc * 64 + 16 * fq;
; #pragma unroll
;         for (int ai = 0; ai < 2; ++ai)
; #pragma unroll
;             for (int m = 0; m < 4; ++m) { const int row = row0 + ai * HALF + m * 16; const float gt = gate[row] * YSCALE; unsigned char* rowp = O + (size_t)row * ldc + col0;
;                 unsigned w[4];
; #pragma unroll
;                 for (int bj = 0; bj < 2; ++bj)
; #pragma unroll
;                     for (int n = 0; n < 2; ++n) { const f32x4 v = acc[ai][bj][m][n] * gt; w[2 * bj + n] = pk4_fp8(clamp448(v[0]), clamp448(v[1]), clamp448(v[2]), clamp448(v[3])); }
;                 *(u32x4*)rowp = (u32x4){w[0], w[1], w[2], w[3]}; }
.LBB0_1629:
	v_lshl_add_u32 v8, s20, 8, v1
	v_ashrrev_i32_e32 v9, 31, v8
	v_lshl_add_u64 v[2:3], v[8:9], 2, s[0:1]
	global_load_dword v228, v[2:3], off
	global_load_dword v229, v[2:3], off offset:64
	global_load_dword v230, v[2:3], off offset:128
	global_load_dword v231, v[2:3], off offset:192
	global_load_dword v232, v[2:3], off offset:512
	global_load_dword v233, v[2:3], off offset:576
	global_load_dword v234, v[2:3], off offset:640
	global_load_dword v235, v[2:3], off offset:704
	v_mov_b32_e32 v10, 0
	v_mov_b32_e32 v11, 0
	v_mov_b32_e32 v12, 0
	v_mov_b32_e32 v13, 0
	v_lshlrev_b64 v[4:5], 10, v[8:9]
	v_lshl_or_b32 v6, s33, 8, v187
	v_ashrrev_i32_e32 v7, 31, v6
	v_or_b32_e32 v14, 16, v8
	v_lshl_add_u64 v[4:5], s[94:95], 0, v[4:5]
	v_ashrrev_i32_e32 v15, 31, v14
	v_lshl_add_u64 v[4:5], v[4:5], 0, v[6:7]
	s_waitcnt vmcnt(0)
	v_mul_f32_e32 v16, 0x42000000, v228
	v_pk_mul_f32 v[18:19], v[160:161], v[16:17] op_sel_hi:[1,0]
	v_pk_mul_f32 v[20:21], v[158:159], v[16:17] op_sel_hi:[1,0]
	v_pk_mul_f32 v[22:23], v[156:157], v[16:17] op_sel_hi:[1,0]
	v_pk_mul_f32 v[24:25], v[154:155], v[16:17] op_sel_hi:[1,0]
	v_pk_mul_f32 v[26:27], v[152:153], v[16:17] op_sel_hi:[1,0]
	v_pk_mul_f32 v[28:29], v[150:151], v[16:17] op_sel_hi:[1,0]
	v_pk_mul_f32 v[30:31], v[148:149], v[16:17] op_sel_hi:[1,0]
	v_pk_mul_f32 v[16:17], v[146:147], v[16:17] op_sel_hi:[1,0]
	v_med3_f32 v9, v20, s41, v193
	v_med3_f32 v20, v21, s41, v193
	v_med3_f32 v21, v24, s41, v193
	v_med3_f32 v24, v25, s41, v193
	v_med3_f32 v25, v28, s41, v193
	v_med3_f32 v28, v29, s41, v193
	v_med3_f32 v16, v16, s41, v193
	v_med3_f32 v17, v17, s41, v193
	v_cvt_pk_fp8_f32 v10, v9, v20
	v_cvt_pk_fp8_f32 v11, v21, v24
	v_cvt_pk_fp8_f32 v12, v25, v28
	v_cvt_pk_fp8_f32 v13, v16, v17
	v_med3_f32 v18, v18, s41, v193
	v_med3_f32 v19, v19, s41, v193
	v_med3_f32 v22, v22, s41, v193
	v_med3_f32 v23, v23, s41, v193
	v_med3_f32 v26, v26, s41, v193
	v_med3_f32 v27, v27, s41, v193
	v_med3_f32 v29, v30, s41, v193
	v_med3_f32 v30, v31, s41, v193
	v_cvt_pk_fp8_f32 v10, v18, v19 op_sel:[0,0,1]
	v_cvt_pk_fp8_f32 v11, v22, v23 op_sel:[0,0,1]
	v_cvt_pk_fp8_f32 v12, v26, v27 op_sel:[0,0,1]
	v_cvt_pk_fp8_f32 v13, v29, v30 op_sel:[0,0,1]
	v_lshl_add_u64 v[16:17], v[14:15], 2, s[0:1]
	v_lshlrev_b64 v[14:15], 10, v[14:15]
	v_lshl_add_u64 v[14:15], s[94:95], 0, v[14:15]
	global_store_dwordx4 v[4:5], v[10:13], off
	s_nop 1
	v_or_b32_e32 v16, 32, v8
	v_mov_b32_e32 v10, 0
	v_mov_b32_e32 v11, 0
	v_mov_b32_e32 v12, 0
	v_mov_b32_e32 v13, 0
	v_ashrrev_i32_e32 v17, 31, v16
	v_lshl_add_u64 v[14:15], v[14:15], 0, v[6:7]
	v_mul_f32_e32 v18, 0x42000000, v229
	v_pk_mul_f32 v[20:21], v[144:145], v[18:19] op_sel_hi:[1,0]
	v_pk_mul_f32 v[22:23], v[142:143], v[18:19] op_sel_hi:[1,0]
	v_pk_mul_f32 v[24:25], v[140:141], v[18:19] op_sel_hi:[1,0]
	v_pk_mul_f32 v[26:27], v[138:139], v[18:19] op_sel_hi:[1,0]
	v_pk_mul_f32 v[28:29], v[136:137], v[18:19] op_sel_hi:[1,0]
	v_pk_mul_f32 v[30:31], v[134:135], v[18:19] op_sel_hi:[1,0]
	v_pk_mul_f32 v[32:33], v[132:133], v[18:19] op_sel_hi:[1,0]
	v_pk_mul_f32 v[18:19], v[130:131], v[18:19] op_sel_hi:[1,0]
	v_med3_f32 v9, v22, s41, v193
	v_med3_f32 v22, v23, s41, v193
	v_med3_f32 v23, v26, s41, v193
	v_med3_f32 v26, v27, s41, v193
	v_med3_f32 v27, v30, s41, v193
	v_med3_f32 v30, v31, s41, v193
	v_med3_f32 v18, v18, s41, v193
	v_med3_f32 v19, v19, s41, v193
	v_cvt_pk_fp8_f32 v10, v9, v22
	v_cvt_pk_fp8_f32 v11, v23, v26
	v_cvt_pk_fp8_f32 v12, v27, v30
	v_cvt_pk_fp8_f32 v13, v18, v19
	v_med3_f32 v20, v20, s41, v193
	v_med3_f32 v21, v21, s41, v193
	v_med3_f32 v24, v24, s41, v193
	v_med3_f32 v25, v25, s41, v193
	v_med3_f32 v28, v28, s41, v193
	v_med3_f32 v29, v29, s41, v193
	v_med3_f32 v31, v32, s41, v193
	v_med3_f32 v32, v33, s41, v193
	v_cvt_pk_fp8_f32 v10, v20, v21 op_sel:[0,0,1]
	v_cvt_pk_fp8_f32 v11, v24, v25 op_sel:[0,0,1]
	v_cvt_pk_fp8_f32 v12, v28, v29 op_sel:[0,0,1]
	v_cvt_pk_fp8_f32 v13, v31, v32 op_sel:[0,0,1]
	v_lshl_add_u64 v[18:19], v[16:17], 2, s[0:1]
	global_store_dwordx4 v[14:15], v[10:13], off
	s_nop 1
	v_or_b32_e32 v14, 48, v8
	v_lshlrev_b64 v[8:9], 10, v[16:17]
	v_mov_b32_e32 v10, 0
	v_mov_b32_e32 v11, 0
	v_mov_b32_e32 v12, 0
	v_mov_b32_e32 v13, 0
	v_lshl_add_u64 v[8:9], s[94:95], 0, v[8:9]
	v_ashrrev_i32_e32 v15, 31, v14
	v_lshl_add_u64 v[8:9], v[8:9], 0, v[6:7]
	v_mul_f32_e32 v16, 0x42000000, v230
	v_pk_mul_f32 v[18:19], v[128:129], v[16:17] op_sel_hi:[1,0]
	v_pk_mul_f32 v[20:21], v[126:127], v[16:17] op_sel_hi:[1,0]
	v_pk_mul_f32 v[22:23], v[124:125], v[16:17] op_sel_hi:[1,0]
	v_pk_mul_f32 v[24:25], v[122:123], v[16:17] op_sel_hi:[1,0]
	v_pk_mul_f32 v[26:27], v[120:121], v[16:17] op_sel_hi:[1,0]
	v_pk_mul_f32 v[28:29], v[118:119], v[16:17] op_sel_hi:[1,0]
	v_pk_mul_f32 v[30:31], v[116:117], v[16:17] op_sel_hi:[1,0]
	v_pk_mul_f32 v[16:17], v[114:115], v[16:17] op_sel_hi:[1,0]
	v_med3_f32 v20, v20, s41, v193
	v_med3_f32 v21, v21, s41, v193
	v_med3_f32 v24, v24, s41, v193
	v_med3_f32 v25, v25, s41, v193
	v_med3_f32 v28, v28, s41, v193
	v_med3_f32 v29, v29, s41, v193
	v_med3_f32 v16, v16, s41, v193
	v_med3_f32 v17, v17, s41, v193
	v_cvt_pk_fp8_f32 v10, v20, v21
	v_cvt_pk_fp8_f32 v11, v24, v25
	v_cvt_pk_fp8_f32 v12, v28, v29
	v_cvt_pk_fp8_f32 v13, v16, v17
	v_med3_f32 v18, v18, s41, v193
	v_med3_f32 v19, v19, s41, v193
	v_med3_f32 v22, v22, s41, v193
	v_med3_f32 v23, v23, s41, v193
	v_med3_f32 v26, v26, s41, v193
	v_med3_f32 v27, v27, s41, v193
	v_med3_f32 v30, v30, s41, v193
	v_med3_f32 v31, v31, s41, v193
	v_cvt_pk_fp8_f32 v10, v18, v19 op_sel:[0,0,1]
	v_cvt_pk_fp8_f32 v11, v22, v23 op_sel:[0,0,1]
	v_cvt_pk_fp8_f32 v12, v26, v27 op_sel:[0,0,1]
	v_cvt_pk_fp8_f32 v13, v30, v31 op_sel:[0,0,1]
; __device__ __forceinline__ unsigned pk4_fp8(float a, float b, float c, float d) { unsigned w = 0u; w = __builtin_amdgcn_cvt_pk_fp8_f32(a, b, w, false); w = __builtin_amdgcn_cvt_pk_fp8_f32(c, d, w, true); return w; }
; __device__ __forceinline__ float clamp448(float v) { return __builtin_amdgcn_fmed3f(v, -448.f, 448.f); }
;     __device__ __forceinline__ void operator()(const f32x4 (&acc)[2][2][4][2], const Unit& u, int wr, int wc, int fr, int fq) const {
;     ...
;             for (int m = 0; m < 4; ++m) { const int row = row0 + ai * HALF + m * 16; const float gt = gate[row] * YSCALE; unsigned char* rowp = O + (size_t)row * ldc + col0;
;                 unsigned w[4];
; #pragma unroll
;                 for (int bj = 0; bj < 2; ++bj)
; #pragma unroll
;                     for (int n = 0; n < 2; ++n) { const f32x4 v = acc[ai][bj][m][n] * gt; w[2 * bj + n] = pk4_fp8(clamp448(v[0]), clamp448(v[1]), clamp448(v[2]), clamp448(v[3])); }
;                 *(u32x4*)rowp = (u32x4){w[0], w[1], w[2], w[3]}; }
	v_lshl_add_u64 v[16:17], v[14:15], 2, s[0:1]
	global_store_dwordx4 v[8:9], v[10:13], off
	s_nop 1
	v_mov_b32_e32 v8, 0
	v_mov_b32_e32 v9, 0
	v_mov_b32_e32 v10, 0
	v_mov_b32_e32 v11, 0
	v_mul_f32_e32 v12, 0x42000000, v231
	v_pk_mul_f32 v[16:17], v[112:113], v[12:13] op_sel_hi:[1,0]
	v_pk_mul_f32 v[18:19], v[110:111], v[12:13] op_sel_hi:[1,0]
	v_pk_mul_f32 v[20:21], v[108:109], v[12:13] op_sel_hi:[1,0]
	v_pk_mul_f32 v[22:23], v[106:107], v[12:13] op_sel_hi:[1,0]
	v_pk_mul_f32 v[24:25], v[104:105], v[12:13] op_sel_hi:[1,0]
	v_pk_mul_f32 v[26:27], v[102:103], v[12:13] op_sel_hi:[1,0]
	v_pk_mul_f32 v[28:29], v[100:101], v[12:13] op_sel_hi:[1,0]
	v_pk_mul_f32 v[12:13], v[98:99], v[12:13] op_sel_hi:[1,0]
	v_med3_f32 v18, v18, s41, v193
	v_med3_f32 v19, v19, s41, v193
	v_med3_f32 v22, v22, s41, v193
	v_med3_f32 v23, v23, s41, v193
	v_med3_f32 v26, v26, s41, v193
	v_med3_f32 v27, v27, s41, v193
	v_med3_f32 v12, v12, s41, v193
	v_med3_f32 v13, v13, s41, v193
	v_cvt_pk_fp8_f32 v8, v18, v19
	v_cvt_pk_fp8_f32 v9, v22, v23
	v_cvt_pk_fp8_f32 v10, v26, v27
	v_cvt_pk_fp8_f32 v11, v12, v13
	v_med3_f32 v16, v16, s41, v193
	v_med3_f32 v17, v17, s41, v193
	v_med3_f32 v20, v20, s41, v193
	v_med3_f32 v21, v21, s41, v193
	v_med3_f32 v24, v24, s41, v193
	v_med3_f32 v25, v25, s41, v193
	v_med3_f32 v28, v28, s41, v193
	v_med3_f32 v29, v29, s41, v193
	v_cvt_pk_fp8_f32 v8, v16, v17 op_sel:[0,0,1]
	v_cvt_pk_fp8_f32 v9, v20, v21 op_sel:[0,0,1]
	v_cvt_pk_fp8_f32 v10, v24, v25 op_sel:[0,0,1]
	v_cvt_pk_fp8_f32 v11, v28, v29 op_sel:[0,0,1]
	v_lshlrev_b64 v[12:13], 10, v[14:15]
	v_lshl_add_u64 v[12:13], s[94:95], 0, v[12:13]
	v_lshl_add_u64 v[6:7], v[12:13], 0, v[6:7]
	global_store_dwordx4 v[6:7], v[8:11], off
	s_nop 1
	v_mov_b32_e32 v6, 0
	v_mov_b32_e32 v7, 0
	v_mov_b32_e32 v8, 0
	v_mov_b32_e32 v9, 0
	v_mul_f32_e32 v10, 0x42000000, v232
	v_pk_mul_f32 v[12:13], v[96:97], v[10:11] op_sel_hi:[1,0]
	v_pk_mul_f32 v[14:15], v[94:95], v[10:11] op_sel_hi:[1,0]
	v_pk_mul_f32 v[16:17], v[92:93], v[10:11] op_sel_hi:[1,0]
	v_pk_mul_f32 v[18:19], v[90:91], v[10:11] op_sel_hi:[1,0]
	v_pk_mul_f32 v[20:21], v[88:89], v[10:11] op_sel_hi:[1,0]
	v_pk_mul_f32 v[22:23], v[86:87], v[10:11] op_sel_hi:[1,0]
	v_pk_mul_f32 v[24:25], v[84:85], v[10:11] op_sel_hi:[1,0]
	v_pk_mul_f32 v[10:11], v[82:83], v[10:11] op_sel_hi:[1,0]
	v_med3_f32 v14, v14, s41, v193
	v_med3_f32 v15, v15, s41, v193
	v_med3_f32 v18, v18, s41, v193
	v_med3_f32 v19, v19, s41, v193
	v_med3_f32 v22, v22, s41, v193
	v_med3_f32 v23, v23, s41, v193
	v_med3_f32 v10, v10, s41, v193
	v_med3_f32 v11, v11, s41, v193
	v_cvt_pk_fp8_f32 v6, v14, v15
	v_cvt_pk_fp8_f32 v7, v18, v19
	v_cvt_pk_fp8_f32 v8, v22, v23
	v_cvt_pk_fp8_f32 v9, v10, v11
	v_med3_f32 v12, v12, s41, v193
	v_med3_f32 v13, v13, s41, v193
	v_med3_f32 v16, v16, s41, v193
	v_med3_f32 v17, v17, s41, v193
	v_med3_f32 v20, v20, s41, v193
	v_med3_f32 v21, v21, s41, v193
	v_med3_f32 v24, v24, s41, v193
	v_med3_f32 v25, v25, s41, v193
	v_cvt_pk_fp8_f32 v6, v12, v13 op_sel:[0,0,1]
	v_cvt_pk_fp8_f32 v7, v16, v17 op_sel:[0,0,1]
	v_cvt_pk_fp8_f32 v8, v20, v21 op_sel:[0,0,1]
	v_cvt_pk_fp8_f32 v9, v24, v25 op_sel:[0,0,1]
	v_add_co_u32_e32 v10, vcc, s42, v4
	s_nop 1
	v_addc_co_u32_e32 v11, vcc, 0, v5, vcc
	global_store_dwordx4 v[10:11], v[6:9], off
	s_nop 1
	v_mul_f32_e32 v10, 0x42000000, v233
	v_pk_mul_f32 v[12:13], v[80:81], v[10:11] op_sel_hi:[1,0]
	v_pk_mul_f32 v[14:15], v[78:79], v[10:11] op_sel_hi:[1,0]
	v_pk_mul_f32 v[16:17], v[76:77], v[10:11] op_sel_hi:[1,0]
	v_pk_mul_f32 v[18:19], v[74:75], v[10:11] op_sel_hi:[1,0]
	v_pk_mul_f32 v[20:21], v[72:73], v[10:11] op_sel_hi:[1,0]
	v_pk_mul_f32 v[22:23], v[70:71], v[10:11] op_sel_hi:[1,0]
	v_pk_mul_f32 v[24:25], v[68:69], v[10:11] op_sel_hi:[1,0]
	v_pk_mul_f32 v[10:11], v[66:67], v[10:11] op_sel_hi:[1,0]
	v_mov_b32_e32 v6, 0
	v_mov_b32_e32 v7, 0
	v_mov_b32_e32 v8, 0
	v_mov_b32_e32 v9, 0
	v_med3_f32 v14, v14, s41, v193
	v_med3_f32 v15, v15, s41, v193
	v_med3_f32 v18, v18, s41, v193
	v_med3_f32 v19, v19, s41, v193
	v_med3_f32 v22, v22, s41, v193
; #define PG8_BAR __builtin_amdgcn_s_barrier()
; __device__ __forceinline__ unsigned pk4_fp8(float a, float b, float c, float d) { unsigned w = 0u; w = __builtin_amdgcn_cvt_pk_fp8_f32(a, b, w, false); w = __builtin_amdgcn_cvt_pk_fp8_f32(c, d, w, true); return w; }
; __device__ __forceinline__ float clamp448(float v) { return __builtin_amdgcn_fmed3f(v, -448.f, 448.f); }
;     ...
;         if (!has_next) break;
; #pragma unroll
;         for (int a = 0; a < 2; ++a)
; #pragma unroll
;             for (int b = 0; b < 2; ++b)
; #pragma unroll
;                 for (int m = 0; m < 4; ++m)
; #pragma unroll
;                     for (int n = 0; n < 2; ++n) acc[a][b][m][n] = (f32x4){0.f, 0.f, 0.f, 0.f};
;         cur = nxt; cA = nA; cB = nB; ++ui;
;         if constexpr (Sched::GATHER) { _Pragma("unroll") for (int h_ = 0; h_ < 2; ++h_) _Pragma("unroll") for (int i_ = 0; i_ < 2; ++i_) vA[h_][i_] = vAn[h_][i_]; }
;         if constexpr (ALIGN_EPI) { if (wr == 1) PG8_BAR; }
;     __device__ __forceinline__ void operator()(const f32x4 (&acc)[2][2][4][2], const Unit& u, int wr, int wc, int fr, int fq) const {
;     ...
;             for (int m = 0; m < 4; ++m) { const int row = row0 + ai * HALF + m * 16; const float gt = gate[row] * YSCALE; unsigned char* rowp = O + (size_t)row * ldc + col0;
;                 unsigned w[4];
; #pragma unroll
;                 for (int bj = 0; bj < 2; ++bj)
; #pragma unroll
;                     for (int n = 0; n < 2; ++n) { const f32x4 v = acc[ai][bj][m][n] * gt; w[2 * bj + n] = pk4_fp8(clamp448(v[0]), clamp448(v[1]), clamp448(v[2]), clamp448(v[3])); }
;                 *(u32x4*)rowp = (u32x4){w[0], w[1], w[2], w[3]}; }
	v_med3_f32 v23, v23, s41, v193
	v_med3_f32 v10, v10, s41, v193
	v_med3_f32 v11, v11, s41, v193
	v_cvt_pk_fp8_f32 v6, v14, v15
	v_cvt_pk_fp8_f32 v7, v18, v19
	v_cvt_pk_fp8_f32 v8, v22, v23
	v_cvt_pk_fp8_f32 v9, v10, v11
	v_med3_f32 v12, v12, s41, v193
	v_med3_f32 v13, v13, s41, v193
	v_med3_f32 v16, v16, s41, v193
	v_med3_f32 v17, v17, s41, v193
	v_med3_f32 v20, v20, s41, v193
	v_med3_f32 v21, v21, s41, v193
	v_med3_f32 v24, v24, s41, v193
	v_med3_f32 v25, v25, s41, v193
	v_cvt_pk_fp8_f32 v6, v12, v13 op_sel:[0,0,1]
	v_cvt_pk_fp8_f32 v7, v16, v17 op_sel:[0,0,1]
	v_cvt_pk_fp8_f32 v8, v20, v21 op_sel:[0,0,1]
	v_cvt_pk_fp8_f32 v9, v24, v25 op_sel:[0,0,1]
	v_add_co_u32_e32 v10, vcc, s43, v4
	s_nop 1
	v_addc_co_u32_e32 v11, vcc, 0, v5, vcc
	global_store_dwordx4 v[10:11], v[6:9], off
	s_nop 1
	v_mul_f32_e32 v10, 0x42000000, v234
	v_pk_mul_f32 v[12:13], v[64:65], v[10:11] op_sel_hi:[1,0]
	v_pk_mul_f32 v[14:15], v[62:63], v[10:11] op_sel_hi:[1,0]
	v_pk_mul_f32 v[16:17], v[60:61], v[10:11] op_sel_hi:[1,0]
	v_pk_mul_f32 v[18:19], v[58:59], v[10:11] op_sel_hi:[1,0]
	v_pk_mul_f32 v[20:21], v[56:57], v[10:11] op_sel_hi:[1,0]
	v_pk_mul_f32 v[22:23], v[54:55], v[10:11] op_sel_hi:[1,0]
	v_pk_mul_f32 v[24:25], v[52:53], v[10:11] op_sel_hi:[1,0]
	v_pk_mul_f32 v[10:11], v[50:51], v[10:11] op_sel_hi:[1,0]
	v_mov_b32_e32 v6, 0
	v_mov_b32_e32 v7, 0
	v_mov_b32_e32 v8, 0
	v_mov_b32_e32 v9, 0
	v_med3_f32 v14, v14, s41, v193
	v_med3_f32 v15, v15, s41, v193
	v_med3_f32 v18, v18, s41, v193
	v_med3_f32 v19, v19, s41, v193
	v_med3_f32 v22, v22, s41, v193
	v_med3_f32 v23, v23, s41, v193
	v_med3_f32 v10, v10, s41, v193
	v_med3_f32 v11, v11, s41, v193
	v_cvt_pk_fp8_f32 v6, v14, v15
	v_cvt_pk_fp8_f32 v7, v18, v19
	v_cvt_pk_fp8_f32 v8, v22, v23
	v_cvt_pk_fp8_f32 v9, v10, v11
	v_med3_f32 v12, v12, s41, v193
	v_med3_f32 v13, v13, s41, v193
	v_med3_f32 v16, v16, s41, v193
	v_med3_f32 v17, v17, s41, v193
	v_med3_f32 v20, v20, s41, v193
	v_med3_f32 v21, v21, s41, v193
	v_med3_f32 v24, v24, s41, v193
	v_med3_f32 v25, v25, s41, v193
	v_cvt_pk_fp8_f32 v6, v12, v13 op_sel:[0,0,1]
	v_cvt_pk_fp8_f32 v7, v16, v17 op_sel:[0,0,1]
	v_cvt_pk_fp8_f32 v8, v20, v21 op_sel:[0,0,1]
	v_cvt_pk_fp8_f32 v9, v24, v25 op_sel:[0,0,1]
	v_add_co_u32_e32 v10, vcc, s44, v4
	s_nop 1
	v_addc_co_u32_e32 v11, vcc, 0, v5, vcc
	global_store_dwordx4 v[10:11], v[6:9], off
	s_nop 1
	v_add_co_u32_e32 v2, vcc, 0x2c000, v4
	v_mov_b32_e32 v6, 0
	v_mov_b32_e32 v7, 0
	v_mov_b32_e32 v8, 0
	v_mov_b32_e32 v9, 0
	v_mul_f32_e32 v4, 0x42000000, v235
	v_pk_mul_f32 v[12:13], v[46:47], v[4:5] op_sel_hi:[1,0]
	v_pk_mul_f32 v[16:17], v[42:43], v[4:5] op_sel_hi:[1,0]
	v_pk_mul_f32 v[20:21], v[38:39], v[4:5] op_sel_hi:[1,0]
	v_pk_mul_f32 v[24:25], v[34:35], v[4:5] op_sel_hi:[1,0]
	v_pk_mul_f32 v[10:11], v[48:49], v[4:5] op_sel_hi:[1,0]
	v_pk_mul_f32 v[14:15], v[44:45], v[4:5] op_sel_hi:[1,0]
	v_pk_mul_f32 v[18:19], v[40:41], v[4:5] op_sel_hi:[1,0]
	v_pk_mul_f32 v[22:23], v[36:37], v[4:5] op_sel_hi:[1,0]
	v_med3_f32 v3, v12, s41, v193
	v_med3_f32 v4, v13, s41, v193
	v_med3_f32 v12, v16, s41, v193
	v_med3_f32 v13, v17, s41, v193
	v_med3_f32 v16, v20, s41, v193
	v_med3_f32 v17, v21, s41, v193
	v_med3_f32 v20, v24, s41, v193
	v_med3_f32 v21, v25, s41, v193
	v_cvt_pk_fp8_f32 v6, v3, v4
	v_cvt_pk_fp8_f32 v7, v12, v13
	v_cvt_pk_fp8_f32 v8, v16, v17
	v_cvt_pk_fp8_f32 v9, v20, v21
	v_med3_f32 v10, v10, s41, v193
	v_med3_f32 v11, v11, s41, v193
	v_med3_f32 v14, v14, s41, v193
	v_med3_f32 v15, v15, s41, v193
	v_med3_f32 v18, v18, s41, v193
	v_med3_f32 v19, v19, s41, v193
	v_med3_f32 v22, v22, s41, v193
	v_med3_f32 v23, v23, s41, v193
	v_cvt_pk_fp8_f32 v6, v10, v11 op_sel:[0,0,1]
	v_cvt_pk_fp8_f32 v7, v14, v15 op_sel:[0,0,1]
	v_cvt_pk_fp8_f32 v8, v18, v19 op_sel:[0,0,1]
	v_cvt_pk_fp8_f32 v9, v22, v23 op_sel:[0,0,1]
	v_addc_co_u32_e32 v3, vcc, 0, v5, vcc
	s_andn2_b64 vcc, exec, s[2:3]
	s_mov_b64 s[2:3], -1
	global_store_dwordx4 v[2:3], v[6:9], off
	s_cbranch_vccnz .LBB0_1622
	s_andn2_b64 vcc, exec, s[6:7]
	s_cbranch_vccnz .LBB0_1621
	s_barrier
	s_branch .LBB0_1621
